# pass A: eight table rows interleaved per FMA group (dependent FMAs eight instructions apart, no extra adds)
# speedup vs baseline: 1.0087x; 1.0030x over previous
.Lpa_tok:
	v_lshlrev_b32_e32 v124, 16, v116
	v_and_b32_e32 v125, 0xffff0000, v116
	v_pk_mul_f32 v[108:109], v[124:125], v[100:101]
	v_lshlrev_b32_e32 v124, 16, v117
	v_and_b32_e32 v125, 0xffff0000, v117
	v_pk_mul_f32 v[110:111], v[124:125], v[102:103]
	v_lshlrev_b32_e32 v124, 16, v118
	v_and_b32_e32 v125, 0xffff0000, v118
	v_pk_mul_f32 v[112:113], v[124:125], v[104:105]
	v_lshlrev_b32_e32 v124, 16, v119
	v_and_b32_e32 v125, 0xffff0000, v119
	v_pk_mul_f32 v[114:115], v[124:125], v[106:107]
	v_add_f32_e32 v16, v108, v109
	v_add_f32_e32 v17, v110, v111
	v_add_f32_e32 v18, v112, v113
	v_add_f32_e32 v19, v114, v115
	v_add_f32_e32 v16, v16, v17
	v_add_f32_e32 v18, v18, v19
	v_add_f32_e32 v16, v16, v18
	s_nop 1
	v_add_f32_dpp v17, v16, v16 quad_perm:[1,0,3,2] row_mask:0xf bank_mask:0xf
	s_nop 1
	v_add_f32_dpp v16, v17, v17 quad_perm:[2,3,0,1] row_mask:0xf bank_mask:0xf
	s_nop 1
	v_add_f32_dpp v17, v16, v16 row_half_mirror row_mask:0xf bank_mask:0xf
	s_nop 1
	v_add_f32_dpp v16, v17, v17 row_ror:8 row_mask:0xf bank_mask:0xf
	v_mov_b32_e32 v17, v16
	s_nop 1
	v_permlane16_swap_b32_e32 v16, v17
	v_add_f32_e32 v16, v16, v17
	v_mov_b32_e32 v17, v16
	s_nop 1
	v_permlane32_swap_b32_e32 v16, v17
	v_add_f32_e32 v16, v16, v17
	s_lshl_b32 s30, s16, 7
	s_add_u32 s28, s22, s30
	s_addc_u32 s29, s23, 0
	v_lshlrev_b32_e32 v19, 1, v1
	s_mov_b64 exec, s[2:3]
	global_store_dword v19, v16, s[28:29]
	s_mov_b64 exec, -1
	v_mov_b32_e32 v120, v122
	v_mov_b32_e32 v121, v123
	s_lshl_b32 s30, s16, 9
	v_lshl_add_u64 v[22:23], v[176:177], 0, s[30:31]
	s_add_i32 s18, s16, 1
	s_min_i32 s18, s18, s24
	s_lshl_b32 s30, s16, 9
	s_add_u32 s36, s40, s30
	s_addc_u32 s37, s41, 0
	s_lshl_b32 s30, s18, 9
	s_add_u32 s38, s40, s30
	s_addc_u32 s39, s41, 0
	s_lshl_b32 s30, s18, 13
	v_lshl_add_u64 v[160:161], v[172:173], 0, s[30:31]
	global_load_dwordx4 v[116:119], v[160:161], off
	s_lshl_b32 s30, s18, 9
	v_lshl_add_u64 v[160:161], v[174:175], 0, s[30:31]
	global_load_dword v122, v[160:161], off
	global_load_dword v123, v[160:161], off offset:256
	s_waitcnt vmcnt(31)
	v_cvt_f32_ubyte0_e32 v124, v24
	v_cvt_f32_ubyte1_e32 v126, v24
	v_cvt_f32_ubyte2_e32 v128, v24
	v_cvt_f32_ubyte3_e32 v130, v24
	v_cvt_f32_ubyte0_e32 v132, v25
	v_cvt_f32_ubyte1_e32 v134, v25
	v_cvt_f32_ubyte2_e32 v136, v25
	v_cvt_f32_ubyte3_e32 v138, v25
	s_waitcnt lgkmcnt(0)
	s_load_dwordx16 s[84:99], s[36:37], 0xc0 glc
	s_lshl_b32 s30, s68, 12
	s_add_u32 s28, s26, s30
	s_addc_u32 s29, s27, 0
	global_load_dwordx2 v[24:25], v162, s[28:29]
	v_cvt_f32_ubyte0_e32 v125, v26
	v_cvt_f32_ubyte1_e32 v127, v26
	v_cvt_f32_ubyte2_e32 v129, v26
	v_cvt_f32_ubyte3_e32 v131, v26
	v_cvt_f32_ubyte0_e32 v133, v27
	v_cvt_f32_ubyte1_e32 v135, v27
	v_cvt_f32_ubyte2_e32 v137, v27
	v_cvt_f32_ubyte3_e32 v139, v27
	s_lshl_b32 s30, s69, 12
	s_add_u32 s28, s26, s30
	s_addc_u32 s29, s27, 0
	global_load_dwordx2 v[26:27], v162, s[28:29]
	v_cvt_f32_ubyte0_e32 v140, v28
	v_cvt_f32_ubyte1_e32 v142, v28
	v_cvt_f32_ubyte2_e32 v144, v28
	v_cvt_f32_ubyte3_e32 v146, v28
	v_cvt_f32_ubyte0_e32 v148, v29
	v_cvt_f32_ubyte1_e32 v150, v29
	v_cvt_f32_ubyte2_e32 v152, v29
	v_cvt_f32_ubyte3_e32 v154, v29
	s_lshl_b32 s30, s70, 12
	s_add_u32 s28, s26, s30
	s_addc_u32 s29, s27, 0
	global_load_dwordx2 v[28:29], v162, s[28:29]
	v_cvt_f32_ubyte0_e32 v141, v30
	v_cvt_f32_ubyte1_e32 v143, v30
	v_cvt_f32_ubyte2_e32 v145, v30
	v_cvt_f32_ubyte3_e32 v147, v30
	v_cvt_f32_ubyte0_e32 v149, v31
	v_cvt_f32_ubyte1_e32 v151, v31
	v_cvt_f32_ubyte2_e32 v153, v31
	v_cvt_f32_ubyte3_e32 v155, v31
	s_lshl_b32 s30, s71, 12
	s_add_u32 s28, s26, s30
	s_addc_u32 s29, s27, 0
	global_load_dwordx2 v[30:31], v162, s[28:29]
	s_waitcnt vmcnt(31)
	v_cvt_f32_ubyte0_e32 v210, v32
	v_cvt_f32_ubyte1_e32 v212, v32
	v_cvt_f32_ubyte2_e32 v214, v32
	v_cvt_f32_ubyte3_e32 v216, v32
	v_cvt_f32_ubyte0_e32 v218, v33
	v_cvt_f32_ubyte1_e32 v220, v33
	v_cvt_f32_ubyte2_e32 v222, v33
	v_cvt_f32_ubyte3_e32 v224, v33
	s_lshl_b32 s30, s72, 12
	s_add_u32 s28, s26, s30
	s_addc_u32 s29, s27, 0
	global_load_dwordx2 v[32:33], v162, s[28:29]
	v_cvt_f32_ubyte0_e32 v211, v34
	v_cvt_f32_ubyte1_e32 v213, v34
	v_cvt_f32_ubyte2_e32 v215, v34
	v_cvt_f32_ubyte3_e32 v217, v34
	v_cvt_f32_ubyte0_e32 v219, v35
	v_cvt_f32_ubyte1_e32 v221, v35
	v_cvt_f32_ubyte2_e32 v223, v35
	v_cvt_f32_ubyte3_e32 v225, v35
	s_lshl_b32 s30, s73, 12
	s_add_u32 s28, s26, s30
	s_addc_u32 s29, s27, 0
	global_load_dwordx2 v[34:35], v162, s[28:29]
	v_cvt_f32_ubyte0_e32 v238, v36
	v_cvt_f32_ubyte1_e32 v240, v36
	v_cvt_f32_ubyte2_e32 v242, v36
	v_cvt_f32_ubyte3_e32 v244, v36
	v_cvt_f32_ubyte0_e32 v246, v37
	v_cvt_f32_ubyte1_e32 v248, v37
	v_cvt_f32_ubyte2_e32 v250, v37
	v_cvt_f32_ubyte3_e32 v252, v37
	s_lshl_b32 s30, s74, 12
	s_add_u32 s28, s26, s30
	s_addc_u32 s29, s27, 0
	global_load_dwordx2 v[36:37], v162, s[28:29]
	v_cvt_f32_ubyte0_e32 v239, v38
	v_cvt_f32_ubyte1_e32 v241, v38
	v_cvt_f32_ubyte2_e32 v243, v38
	v_cvt_f32_ubyte3_e32 v245, v38
	v_cvt_f32_ubyte0_e32 v247, v39
	v_cvt_f32_ubyte1_e32 v249, v39
	v_cvt_f32_ubyte2_e32 v251, v39
	v_cvt_f32_ubyte3_e32 v253, v39
	s_lshl_b32 s30, s75, 12
	s_add_u32 s28, s26, s30
	s_addc_u32 s29, s27, 0
	global_load_dwordx2 v[38:39], v162, s[28:29]
	v_mul_f32_e32 v178, v124, v108
	v_mul_f32_e32 v179, v125, v108
	v_mul_f32_e32 v180, v140, v108
	v_mul_f32_e32 v181, v141, v108
	v_mul_f32_e32 v182, v210, v108
	v_mul_f32_e32 v183, v211, v108
	v_mul_f32_e32 v184, v238, v108
	v_mul_f32_e32 v185, v239, v108
	v_fmac_f32_e32 v178, v126, v109
	v_fmac_f32_e32 v179, v127, v109
	v_fmac_f32_e32 v180, v142, v109
	v_fmac_f32_e32 v181, v143, v109
	v_fmac_f32_e32 v182, v212, v109
	v_fmac_f32_e32 v183, v213, v109
	v_fmac_f32_e32 v184, v240, v109
	v_fmac_f32_e32 v185, v241, v109
	v_fmac_f32_e32 v178, v128, v110
	v_fmac_f32_e32 v179, v129, v110
	v_fmac_f32_e32 v180, v144, v110
	v_fmac_f32_e32 v181, v145, v110
	v_fmac_f32_e32 v182, v214, v110
	v_fmac_f32_e32 v183, v215, v110
	v_fmac_f32_e32 v184, v242, v110
	v_fmac_f32_e32 v185, v243, v110
	v_fmac_f32_e32 v178, v130, v111
	v_fmac_f32_e32 v179, v131, v111
	v_fmac_f32_e32 v180, v146, v111
	v_fmac_f32_e32 v181, v147, v111
	v_fmac_f32_e32 v182, v216, v111
	v_fmac_f32_e32 v183, v217, v111
	v_fmac_f32_e32 v184, v244, v111
	v_fmac_f32_e32 v185, v245, v111
	v_fmac_f32_e32 v178, v132, v112
	v_fmac_f32_e32 v179, v133, v112
	v_fmac_f32_e32 v180, v148, v112
	v_fmac_f32_e32 v181, v149, v112
	v_fmac_f32_e32 v182, v218, v112
	v_fmac_f32_e32 v183, v219, v112
	v_fmac_f32_e32 v184, v246, v112
	v_fmac_f32_e32 v185, v247, v112
	v_fmac_f32_e32 v178, v134, v113
	v_fmac_f32_e32 v179, v135, v113
	v_fmac_f32_e32 v180, v150, v113
	v_fmac_f32_e32 v181, v151, v113
	v_fmac_f32_e32 v182, v220, v113
	v_fmac_f32_e32 v183, v221, v113
	v_fmac_f32_e32 v184, v248, v113
	v_fmac_f32_e32 v185, v249, v113
	v_fmac_f32_e32 v178, v136, v114
	v_fmac_f32_e32 v179, v137, v114
	v_fmac_f32_e32 v180, v152, v114
	v_fmac_f32_e32 v181, v153, v114
	v_fmac_f32_e32 v182, v222, v114
	v_fmac_f32_e32 v183, v223, v114
	v_fmac_f32_e32 v184, v250, v114
	v_fmac_f32_e32 v185, v251, v114
	v_fmac_f32_e32 v178, v138, v115
	v_fmac_f32_e32 v179, v139, v115
	v_fmac_f32_e32 v180, v154, v115
	v_fmac_f32_e32 v181, v155, v115
	v_fmac_f32_e32 v182, v224, v115
	v_fmac_f32_e32 v183, v225, v115
	v_fmac_f32_e32 v184, v252, v115
	v_fmac_f32_e32 v185, v253, v115
	s_waitcnt vmcnt(31)
	v_cvt_f32_ubyte0_e32 v124, v40
	v_cvt_f32_ubyte1_e32 v126, v40
	v_cvt_f32_ubyte2_e32 v128, v40
	v_cvt_f32_ubyte3_e32 v130, v40
	v_cvt_f32_ubyte0_e32 v132, v41
	v_cvt_f32_ubyte1_e32 v134, v41
	v_cvt_f32_ubyte2_e32 v136, v41
	v_cvt_f32_ubyte3_e32 v138, v41
	s_lshl_b32 s30, s76, 12
	s_add_u32 s28, s26, s30
	s_addc_u32 s29, s27, 0
	global_load_dwordx2 v[40:41], v162, s[28:29]
	v_cvt_f32_ubyte0_e32 v125, v42
	v_cvt_f32_ubyte1_e32 v127, v42
	v_cvt_f32_ubyte2_e32 v129, v42
	v_cvt_f32_ubyte3_e32 v131, v42
	v_cvt_f32_ubyte0_e32 v133, v43
	v_cvt_f32_ubyte1_e32 v135, v43
	v_cvt_f32_ubyte2_e32 v137, v43
	v_cvt_f32_ubyte3_e32 v139, v43
	s_lshl_b32 s30, s77, 12
	s_add_u32 s28, s26, s30
	s_addc_u32 s29, s27, 0
	global_load_dwordx2 v[42:43], v162, s[28:29]
	v_cvt_f32_ubyte0_e32 v140, v44
	v_cvt_f32_ubyte1_e32 v142, v44
	v_cvt_f32_ubyte2_e32 v144, v44
	v_cvt_f32_ubyte3_e32 v146, v44
	v_cvt_f32_ubyte0_e32 v148, v45
	v_cvt_f32_ubyte1_e32 v150, v45
	v_cvt_f32_ubyte2_e32 v152, v45
	v_cvt_f32_ubyte3_e32 v154, v45
	s_lshl_b32 s30, s78, 12
	s_add_u32 s28, s26, s30
	s_addc_u32 s29, s27, 0
	global_load_dwordx2 v[44:45], v162, s[28:29]
	v_cvt_f32_ubyte0_e32 v141, v46
	v_cvt_f32_ubyte1_e32 v143, v46
	v_cvt_f32_ubyte2_e32 v145, v46
	v_cvt_f32_ubyte3_e32 v147, v46
	v_cvt_f32_ubyte0_e32 v149, v47
	v_cvt_f32_ubyte1_e32 v151, v47
	v_cvt_f32_ubyte2_e32 v153, v47
	v_cvt_f32_ubyte3_e32 v155, v47
	s_lshl_b32 s30, s79, 12
	s_add_u32 s28, s26, s30
	s_addc_u32 s29, s27, 0
	global_load_dwordx2 v[46:47], v162, s[28:29]
	s_waitcnt vmcnt(31)
	v_cvt_f32_ubyte0_e32 v210, v48
	v_cvt_f32_ubyte1_e32 v212, v48
	v_cvt_f32_ubyte2_e32 v214, v48
	v_cvt_f32_ubyte3_e32 v216, v48
	v_cvt_f32_ubyte0_e32 v218, v49
	v_cvt_f32_ubyte1_e32 v220, v49
	v_cvt_f32_ubyte2_e32 v222, v49
	v_cvt_f32_ubyte3_e32 v224, v49
	s_lshl_b32 s30, s80, 12
	s_add_u32 s28, s26, s30
	s_addc_u32 s29, s27, 0
	global_load_dwordx2 v[48:49], v162, s[28:29]
	v_cvt_f32_ubyte0_e32 v211, v50
	v_cvt_f32_ubyte1_e32 v213, v50
	v_cvt_f32_ubyte2_e32 v215, v50
	v_cvt_f32_ubyte3_e32 v217, v50
	v_cvt_f32_ubyte0_e32 v219, v51
	v_cvt_f32_ubyte1_e32 v221, v51
	v_cvt_f32_ubyte2_e32 v223, v51
	v_cvt_f32_ubyte3_e32 v225, v51
	s_lshl_b32 s30, s81, 12
	s_add_u32 s28, s26, s30
	s_addc_u32 s29, s27, 0
	global_load_dwordx2 v[50:51], v162, s[28:29]
	v_cvt_f32_ubyte0_e32 v238, v52
	v_cvt_f32_ubyte1_e32 v240, v52
	v_cvt_f32_ubyte2_e32 v242, v52
	v_cvt_f32_ubyte3_e32 v244, v52
	v_cvt_f32_ubyte0_e32 v246, v53
	v_cvt_f32_ubyte1_e32 v248, v53
	v_cvt_f32_ubyte2_e32 v250, v53
	v_cvt_f32_ubyte3_e32 v252, v53
	s_lshl_b32 s30, s82, 12
	s_add_u32 s28, s26, s30
	s_addc_u32 s29, s27, 0
	global_load_dwordx2 v[52:53], v162, s[28:29]
	v_cvt_f32_ubyte0_e32 v239, v54
	v_cvt_f32_ubyte1_e32 v241, v54
	v_cvt_f32_ubyte2_e32 v243, v54
	v_cvt_f32_ubyte3_e32 v245, v54
	v_cvt_f32_ubyte0_e32 v247, v55
	v_cvt_f32_ubyte1_e32 v249, v55
	v_cvt_f32_ubyte2_e32 v251, v55
	v_cvt_f32_ubyte3_e32 v253, v55
	s_lshl_b32 s30, s83, 12
	s_add_u32 s28, s26, s30
	s_addc_u32 s29, s27, 0
	global_load_dwordx2 v[54:55], v162, s[28:29]
	v_mul_f32_e32 v186, v124, v108
	v_mul_f32_e32 v187, v125, v108
	v_mul_f32_e32 v188, v140, v108
	v_mul_f32_e32 v189, v141, v108
	v_mul_f32_e32 v190, v210, v108
	v_mul_f32_e32 v191, v211, v108
	v_mul_f32_e32 v192, v238, v108
	v_mul_f32_e32 v193, v239, v108
	v_fmac_f32_e32 v186, v126, v109
	v_fmac_f32_e32 v187, v127, v109
	v_fmac_f32_e32 v188, v142, v109
	v_fmac_f32_e32 v189, v143, v109
	v_fmac_f32_e32 v190, v212, v109
	v_fmac_f32_e32 v191, v213, v109
	v_fmac_f32_e32 v192, v240, v109
	v_fmac_f32_e32 v193, v241, v109
	v_fmac_f32_e32 v186, v128, v110
	v_fmac_f32_e32 v187, v129, v110
	v_fmac_f32_e32 v188, v144, v110
	v_fmac_f32_e32 v189, v145, v110
	v_fmac_f32_e32 v190, v214, v110
	v_fmac_f32_e32 v191, v215, v110
	v_fmac_f32_e32 v192, v242, v110
	v_fmac_f32_e32 v193, v243, v110
	v_fmac_f32_e32 v186, v130, v111
	v_fmac_f32_e32 v187, v131, v111
	v_fmac_f32_e32 v188, v146, v111
	v_fmac_f32_e32 v189, v147, v111
	v_fmac_f32_e32 v190, v216, v111
	v_fmac_f32_e32 v191, v217, v111
	v_fmac_f32_e32 v192, v244, v111
	v_fmac_f32_e32 v193, v245, v111
	v_fmac_f32_e32 v186, v132, v112
	v_fmac_f32_e32 v187, v133, v112
	v_fmac_f32_e32 v188, v148, v112
	v_fmac_f32_e32 v189, v149, v112
	v_fmac_f32_e32 v190, v218, v112
	v_fmac_f32_e32 v191, v219, v112
	v_fmac_f32_e32 v192, v246, v112
	v_fmac_f32_e32 v193, v247, v112
	v_fmac_f32_e32 v186, v134, v113
	v_fmac_f32_e32 v187, v135, v113
	v_fmac_f32_e32 v188, v150, v113
	v_fmac_f32_e32 v189, v151, v113
	v_fmac_f32_e32 v190, v220, v113
	v_fmac_f32_e32 v191, v221, v113
	v_fmac_f32_e32 v192, v248, v113
	v_fmac_f32_e32 v193, v249, v113
	v_fmac_f32_e32 v186, v136, v114
	v_fmac_f32_e32 v187, v137, v114
	v_fmac_f32_e32 v188, v152, v114
	v_fmac_f32_e32 v189, v153, v114
	v_fmac_f32_e32 v190, v222, v114
	v_fmac_f32_e32 v191, v223, v114
	v_fmac_f32_e32 v192, v250, v114
	v_fmac_f32_e32 v193, v251, v114
	v_fmac_f32_e32 v186, v138, v115
	v_fmac_f32_e32 v187, v139, v115
	v_fmac_f32_e32 v188, v154, v115
	v_fmac_f32_e32 v189, v155, v115
	v_fmac_f32_e32 v190, v224, v115
	v_fmac_f32_e32 v191, v225, v115
	v_fmac_f32_e32 v192, v252, v115
	v_fmac_f32_e32 v193, v253, v115
	s_waitcnt vmcnt(31)
	v_cvt_f32_ubyte0_e32 v124, v56
	v_cvt_f32_ubyte1_e32 v126, v56
	v_cvt_f32_ubyte2_e32 v128, v56
	v_cvt_f32_ubyte3_e32 v130, v56
	v_cvt_f32_ubyte0_e32 v132, v57
	v_cvt_f32_ubyte1_e32 v134, v57
	v_cvt_f32_ubyte2_e32 v136, v57
	v_cvt_f32_ubyte3_e32 v138, v57
	s_waitcnt lgkmcnt(0)
	s_load_dwordx16 s[68:83], s[36:37], 0x100 glc
	s_lshl_b32 s30, s84, 12
	s_add_u32 s28, s26, s30
	s_addc_u32 s29, s27, 0
	global_load_dwordx2 v[56:57], v162, s[28:29]
	v_cvt_f32_ubyte0_e32 v125, v58
	v_cvt_f32_ubyte1_e32 v127, v58
	v_cvt_f32_ubyte2_e32 v129, v58
	v_cvt_f32_ubyte3_e32 v131, v58
	v_cvt_f32_ubyte0_e32 v133, v59
	v_cvt_f32_ubyte1_e32 v135, v59
	v_cvt_f32_ubyte2_e32 v137, v59
	v_cvt_f32_ubyte3_e32 v139, v59
	s_lshl_b32 s30, s85, 12
	s_add_u32 s28, s26, s30
	s_addc_u32 s29, s27, 0
	global_load_dwordx2 v[58:59], v162, s[28:29]
	v_cvt_f32_ubyte0_e32 v140, v60
	v_cvt_f32_ubyte1_e32 v142, v60
	v_cvt_f32_ubyte2_e32 v144, v60
	v_cvt_f32_ubyte3_e32 v146, v60
	v_cvt_f32_ubyte0_e32 v148, v61
	v_cvt_f32_ubyte1_e32 v150, v61
	v_cvt_f32_ubyte2_e32 v152, v61
	v_cvt_f32_ubyte3_e32 v154, v61
	s_lshl_b32 s30, s86, 12
	s_add_u32 s28, s26, s30
	s_addc_u32 s29, s27, 0
	global_load_dwordx2 v[60:61], v162, s[28:29]
	v_cvt_f32_ubyte0_e32 v141, v62
	v_cvt_f32_ubyte1_e32 v143, v62
	v_cvt_f32_ubyte2_e32 v145, v62
	v_cvt_f32_ubyte3_e32 v147, v62
	v_cvt_f32_ubyte0_e32 v149, v63
	v_cvt_f32_ubyte1_e32 v151, v63
	v_cvt_f32_ubyte2_e32 v153, v63
	v_cvt_f32_ubyte3_e32 v155, v63
	s_lshl_b32 s30, s87, 12
	s_add_u32 s28, s26, s30
	s_addc_u32 s29, s27, 0
	global_load_dwordx2 v[62:63], v162, s[28:29]
	s_waitcnt vmcnt(31)
	v_cvt_f32_ubyte0_e32 v210, v64
	v_cvt_f32_ubyte1_e32 v212, v64
	v_cvt_f32_ubyte2_e32 v214, v64
	v_cvt_f32_ubyte3_e32 v216, v64
	v_cvt_f32_ubyte0_e32 v218, v65
	v_cvt_f32_ubyte1_e32 v220, v65
	v_cvt_f32_ubyte2_e32 v222, v65
	v_cvt_f32_ubyte3_e32 v224, v65
	s_lshl_b32 s30, s88, 12
	s_add_u32 s28, s26, s30
	s_addc_u32 s29, s27, 0
	global_load_dwordx2 v[64:65], v162, s[28:29]
	v_cvt_f32_ubyte0_e32 v211, v66
	v_cvt_f32_ubyte1_e32 v213, v66
	v_cvt_f32_ubyte2_e32 v215, v66
	v_cvt_f32_ubyte3_e32 v217, v66
	v_cvt_f32_ubyte0_e32 v219, v67
	v_cvt_f32_ubyte1_e32 v221, v67
	v_cvt_f32_ubyte2_e32 v223, v67
	v_cvt_f32_ubyte3_e32 v225, v67
	s_lshl_b32 s30, s89, 12
	s_add_u32 s28, s26, s30
	s_addc_u32 s29, s27, 0
	global_load_dwordx2 v[66:67], v162, s[28:29]
	v_cvt_f32_ubyte0_e32 v238, v68
	v_cvt_f32_ubyte1_e32 v240, v68
	v_cvt_f32_ubyte2_e32 v242, v68
	v_cvt_f32_ubyte3_e32 v244, v68
	v_cvt_f32_ubyte0_e32 v246, v69
	v_cvt_f32_ubyte1_e32 v248, v69
	v_cvt_f32_ubyte2_e32 v250, v69
	v_cvt_f32_ubyte3_e32 v252, v69
	s_lshl_b32 s30, s90, 12
	s_add_u32 s28, s26, s30
	s_addc_u32 s29, s27, 0
	global_load_dwordx2 v[68:69], v162, s[28:29]
	v_cvt_f32_ubyte0_e32 v239, v70
	v_cvt_f32_ubyte1_e32 v241, v70
	v_cvt_f32_ubyte2_e32 v243, v70
	v_cvt_f32_ubyte3_e32 v245, v70
	v_cvt_f32_ubyte0_e32 v247, v71
	v_cvt_f32_ubyte1_e32 v249, v71
	v_cvt_f32_ubyte2_e32 v251, v71
	v_cvt_f32_ubyte3_e32 v253, v71
	s_lshl_b32 s30, s91, 12
	s_add_u32 s28, s26, s30
	s_addc_u32 s29, s27, 0
	global_load_dwordx2 v[70:71], v162, s[28:29]
	v_mul_f32_e32 v194, v124, v108
	v_mul_f32_e32 v195, v125, v108
	v_mul_f32_e32 v196, v140, v108
	v_mul_f32_e32 v197, v141, v108
	v_mul_f32_e32 v198, v210, v108
	v_mul_f32_e32 v199, v211, v108
	v_mul_f32_e32 v200, v238, v108
	v_mul_f32_e32 v201, v239, v108
	v_fmac_f32_e32 v194, v126, v109
	v_fmac_f32_e32 v195, v127, v109
	v_fmac_f32_e32 v196, v142, v109
	v_fmac_f32_e32 v197, v143, v109
	v_fmac_f32_e32 v198, v212, v109
	v_fmac_f32_e32 v199, v213, v109
	v_fmac_f32_e32 v200, v240, v109
	v_fmac_f32_e32 v201, v241, v109
	v_fmac_f32_e32 v194, v128, v110
	v_fmac_f32_e32 v195, v129, v110
	v_fmac_f32_e32 v196, v144, v110
	v_fmac_f32_e32 v197, v145, v110
	v_fmac_f32_e32 v198, v214, v110
	v_fmac_f32_e32 v199, v215, v110
	v_fmac_f32_e32 v200, v242, v110
	v_fmac_f32_e32 v201, v243, v110
	v_fmac_f32_e32 v194, v130, v111
	v_fmac_f32_e32 v195, v131, v111
	v_fmac_f32_e32 v196, v146, v111
	v_fmac_f32_e32 v197, v147, v111
	v_fmac_f32_e32 v198, v216, v111
	v_fmac_f32_e32 v199, v217, v111
	v_fmac_f32_e32 v200, v244, v111
	v_fmac_f32_e32 v201, v245, v111
	v_fmac_f32_e32 v194, v132, v112
	v_fmac_f32_e32 v195, v133, v112
	v_fmac_f32_e32 v196, v148, v112
	v_fmac_f32_e32 v197, v149, v112
	v_fmac_f32_e32 v198, v218, v112
	v_fmac_f32_e32 v199, v219, v112
	v_fmac_f32_e32 v200, v246, v112
	v_fmac_f32_e32 v201, v247, v112
	v_fmac_f32_e32 v194, v134, v113
	v_fmac_f32_e32 v195, v135, v113
	v_fmac_f32_e32 v196, v150, v113
	v_fmac_f32_e32 v197, v151, v113
	v_fmac_f32_e32 v198, v220, v113
	v_fmac_f32_e32 v199, v221, v113
	v_fmac_f32_e32 v200, v248, v113
	v_fmac_f32_e32 v201, v249, v113
	v_fmac_f32_e32 v194, v136, v114
	v_fmac_f32_e32 v195, v137, v114
	v_fmac_f32_e32 v196, v152, v114
	v_fmac_f32_e32 v197, v153, v114
	v_fmac_f32_e32 v198, v222, v114
	v_fmac_f32_e32 v199, v223, v114
	v_fmac_f32_e32 v200, v250, v114
	v_fmac_f32_e32 v201, v251, v114
	v_fmac_f32_e32 v194, v138, v115
	v_fmac_f32_e32 v195, v139, v115
	v_fmac_f32_e32 v196, v154, v115
	v_fmac_f32_e32 v197, v155, v115
	v_fmac_f32_e32 v198, v224, v115
	v_fmac_f32_e32 v199, v225, v115
	v_fmac_f32_e32 v200, v252, v115
	v_fmac_f32_e32 v201, v253, v115
	s_waitcnt vmcnt(31)
	v_cvt_f32_ubyte0_e32 v124, v72
	v_cvt_f32_ubyte1_e32 v126, v72
	v_cvt_f32_ubyte2_e32 v128, v72
	v_cvt_f32_ubyte3_e32 v130, v72
	v_cvt_f32_ubyte0_e32 v132, v73
	v_cvt_f32_ubyte1_e32 v134, v73
	v_cvt_f32_ubyte2_e32 v136, v73
	v_cvt_f32_ubyte3_e32 v138, v73
	s_lshl_b32 s30, s92, 12
	s_add_u32 s28, s26, s30
	s_addc_u32 s29, s27, 0
	global_load_dwordx2 v[72:73], v162, s[28:29]
	v_cvt_f32_ubyte0_e32 v125, v74
	v_cvt_f32_ubyte1_e32 v127, v74
	v_cvt_f32_ubyte2_e32 v129, v74
	v_cvt_f32_ubyte3_e32 v131, v74
	v_cvt_f32_ubyte0_e32 v133, v75
	v_cvt_f32_ubyte1_e32 v135, v75
	v_cvt_f32_ubyte2_e32 v137, v75
	v_cvt_f32_ubyte3_e32 v139, v75
	s_lshl_b32 s30, s93, 12
	s_add_u32 s28, s26, s30
	s_addc_u32 s29, s27, 0
	global_load_dwordx2 v[74:75], v162, s[28:29]
	v_cvt_f32_ubyte0_e32 v140, v76
	v_cvt_f32_ubyte1_e32 v142, v76
	v_cvt_f32_ubyte2_e32 v144, v76
	v_cvt_f32_ubyte3_e32 v146, v76
	v_cvt_f32_ubyte0_e32 v148, v77
	v_cvt_f32_ubyte1_e32 v150, v77
	v_cvt_f32_ubyte2_e32 v152, v77
	v_cvt_f32_ubyte3_e32 v154, v77
	s_lshl_b32 s30, s94, 12
	s_add_u32 s28, s26, s30
	s_addc_u32 s29, s27, 0
	global_load_dwordx2 v[76:77], v162, s[28:29]
	v_cvt_f32_ubyte0_e32 v141, v78
	v_cvt_f32_ubyte1_e32 v143, v78
	v_cvt_f32_ubyte2_e32 v145, v78
	v_cvt_f32_ubyte3_e32 v147, v78
	v_cvt_f32_ubyte0_e32 v149, v79
	v_cvt_f32_ubyte1_e32 v151, v79
	v_cvt_f32_ubyte2_e32 v153, v79
	v_cvt_f32_ubyte3_e32 v155, v79
	s_lshl_b32 s30, s95, 12
	s_add_u32 s28, s26, s30
	s_addc_u32 s29, s27, 0
	global_load_dwordx2 v[78:79], v162, s[28:29]
	s_waitcnt vmcnt(31)
	v_cvt_f32_ubyte0_e32 v210, v80
	v_cvt_f32_ubyte1_e32 v212, v80
	v_cvt_f32_ubyte2_e32 v214, v80
	v_cvt_f32_ubyte3_e32 v216, v80
	v_cvt_f32_ubyte0_e32 v218, v81
	v_cvt_f32_ubyte1_e32 v220, v81
	v_cvt_f32_ubyte2_e32 v222, v81
	v_cvt_f32_ubyte3_e32 v224, v81
	s_lshl_b32 s30, s96, 12
	s_add_u32 s28, s26, s30
	s_addc_u32 s29, s27, 0
	global_load_dwordx2 v[80:81], v162, s[28:29]
	v_cvt_f32_ubyte0_e32 v211, v82
	v_cvt_f32_ubyte1_e32 v213, v82
	v_cvt_f32_ubyte2_e32 v215, v82
	v_cvt_f32_ubyte3_e32 v217, v82
	v_cvt_f32_ubyte0_e32 v219, v83
	v_cvt_f32_ubyte1_e32 v221, v83
	v_cvt_f32_ubyte2_e32 v223, v83
	v_cvt_f32_ubyte3_e32 v225, v83
	s_lshl_b32 s30, s97, 12
	s_add_u32 s28, s26, s30
	s_addc_u32 s29, s27, 0
	global_load_dwordx2 v[82:83], v162, s[28:29]
	v_cvt_f32_ubyte0_e32 v238, v84
	v_cvt_f32_ubyte1_e32 v240, v84
	v_cvt_f32_ubyte2_e32 v242, v84
	v_cvt_f32_ubyte3_e32 v244, v84
	v_cvt_f32_ubyte0_e32 v246, v85
	v_cvt_f32_ubyte1_e32 v248, v85
	v_cvt_f32_ubyte2_e32 v250, v85
	v_cvt_f32_ubyte3_e32 v252, v85
	s_lshl_b32 s30, s98, 12
	s_add_u32 s28, s26, s30
	s_addc_u32 s29, s27, 0
	global_load_dwordx2 v[84:85], v162, s[28:29]
	v_cvt_f32_ubyte0_e32 v239, v86
	v_cvt_f32_ubyte1_e32 v241, v86
	v_cvt_f32_ubyte2_e32 v243, v86
	v_cvt_f32_ubyte3_e32 v245, v86
	v_cvt_f32_ubyte0_e32 v247, v87
	v_cvt_f32_ubyte1_e32 v249, v87
	v_cvt_f32_ubyte2_e32 v251, v87
	v_cvt_f32_ubyte3_e32 v253, v87
	s_lshl_b32 s30, s99, 12
	s_add_u32 s28, s26, s30
	s_addc_u32 s29, s27, 0
	global_load_dwordx2 v[86:87], v162, s[28:29]
	v_mul_f32_e32 v202, v124, v108
	v_mul_f32_e32 v203, v125, v108
	v_mul_f32_e32 v204, v140, v108
	v_mul_f32_e32 v205, v141, v108
	v_mul_f32_e32 v206, v210, v108
	v_mul_f32_e32 v207, v211, v108
	v_mul_f32_e32 v208, v238, v108
	v_mul_f32_e32 v209, v239, v108
	v_fmac_f32_e32 v202, v126, v109
	v_fmac_f32_e32 v203, v127, v109
	v_fmac_f32_e32 v204, v142, v109
	v_fmac_f32_e32 v205, v143, v109
	v_fmac_f32_e32 v206, v212, v109
	v_fmac_f32_e32 v207, v213, v109
	v_fmac_f32_e32 v208, v240, v109
	v_fmac_f32_e32 v209, v241, v109
	v_fmac_f32_e32 v202, v128, v110
	v_fmac_f32_e32 v203, v129, v110
	v_fmac_f32_e32 v204, v144, v110
	v_fmac_f32_e32 v205, v145, v110
	v_fmac_f32_e32 v206, v214, v110
	v_fmac_f32_e32 v207, v215, v110
	v_fmac_f32_e32 v208, v242, v110
	v_fmac_f32_e32 v209, v243, v110
	v_fmac_f32_e32 v202, v130, v111
	v_fmac_f32_e32 v203, v131, v111
	v_fmac_f32_e32 v204, v146, v111
	v_fmac_f32_e32 v205, v147, v111
	v_fmac_f32_e32 v206, v216, v111
	v_fmac_f32_e32 v207, v217, v111
	v_fmac_f32_e32 v208, v244, v111
	v_fmac_f32_e32 v209, v245, v111
	v_fmac_f32_e32 v202, v132, v112
	v_fmac_f32_e32 v203, v133, v112
	v_fmac_f32_e32 v204, v148, v112
	v_fmac_f32_e32 v205, v149, v112
	v_fmac_f32_e32 v206, v218, v112
	v_fmac_f32_e32 v207, v219, v112
	v_fmac_f32_e32 v208, v246, v112
	v_fmac_f32_e32 v209, v247, v112
	v_fmac_f32_e32 v202, v134, v113
	v_fmac_f32_e32 v203, v135, v113
	v_fmac_f32_e32 v204, v150, v113
	v_fmac_f32_e32 v205, v151, v113
	v_fmac_f32_e32 v206, v220, v113
	v_fmac_f32_e32 v207, v221, v113
	v_fmac_f32_e32 v208, v248, v113
	v_fmac_f32_e32 v209, v249, v113
	v_fmac_f32_e32 v202, v136, v114
	v_fmac_f32_e32 v203, v137, v114
	v_fmac_f32_e32 v204, v152, v114
	v_fmac_f32_e32 v205, v153, v114
	v_fmac_f32_e32 v206, v222, v114
	v_fmac_f32_e32 v207, v223, v114
	v_fmac_f32_e32 v208, v250, v114
	v_fmac_f32_e32 v209, v251, v114
	v_fmac_f32_e32 v202, v138, v115
	v_fmac_f32_e32 v203, v139, v115
	v_fmac_f32_e32 v204, v154, v115
	v_fmac_f32_e32 v205, v155, v115
	v_fmac_f32_e32 v206, v224, v115
	v_fmac_f32_e32 v207, v225, v115
	v_fmac_f32_e32 v208, v252, v115
	v_fmac_f32_e32 v209, v253, v115
	v_permlane32_swap_b32_e32 v178, v194
	v_permlane32_swap_b32_e32 v179, v195
	v_permlane32_swap_b32_e32 v180, v196
	v_permlane32_swap_b32_e32 v181, v197
	v_permlane32_swap_b32_e32 v182, v198
	v_permlane32_swap_b32_e32 v183, v199
	v_permlane32_swap_b32_e32 v184, v200
	v_permlane32_swap_b32_e32 v185, v201
	v_permlane32_swap_b32_e32 v186, v202
	v_permlane32_swap_b32_e32 v187, v203
	v_permlane32_swap_b32_e32 v188, v204
	v_permlane32_swap_b32_e32 v189, v205
	v_permlane32_swap_b32_e32 v190, v206
	v_permlane32_swap_b32_e32 v191, v207
	v_permlane32_swap_b32_e32 v192, v208
	v_permlane32_swap_b32_e32 v193, v209
	v_add_f32_e32 v178, v178, v194
	v_add_f32_e32 v179, v179, v195
	v_add_f32_e32 v180, v180, v196
	v_add_f32_e32 v181, v181, v197
	v_add_f32_e32 v182, v182, v198
	v_add_f32_e32 v183, v183, v199
	v_add_f32_e32 v184, v184, v200
	v_add_f32_e32 v185, v185, v201
	v_add_f32_e32 v186, v186, v202
	v_add_f32_e32 v187, v187, v203
	v_add_f32_e32 v188, v188, v204
	v_add_f32_e32 v189, v189, v205
	v_add_f32_e32 v190, v190, v206
	v_add_f32_e32 v191, v191, v207
	v_add_f32_e32 v192, v192, v208
	v_add_f32_e32 v193, v193, v209
	v_permlane16_swap_b32_e32 v178, v186
	v_permlane16_swap_b32_e32 v179, v187
	v_permlane16_swap_b32_e32 v180, v188
	v_permlane16_swap_b32_e32 v181, v189
	v_permlane16_swap_b32_e32 v182, v190
	v_permlane16_swap_b32_e32 v183, v191
	v_permlane16_swap_b32_e32 v184, v192
	v_permlane16_swap_b32_e32 v185, v193
	v_add_f32_e32 v178, v178, v186
	v_add_f32_e32 v179, v179, v187
	v_add_f32_e32 v180, v180, v188
	v_add_f32_e32 v181, v181, v189
	v_add_f32_e32 v182, v182, v190
	v_add_f32_e32 v183, v183, v191
	v_add_f32_e32 v184, v184, v192
	v_add_f32_e32 v185, v185, v193
	v_cndmask_b32_e64 v2, v178, v182, s[8:9]
	v_cndmask_b32_e64 v3, v179, v183, s[8:9]
	v_cndmask_b32_e64 v4, v180, v184, s[8:9]
	v_cndmask_b32_e64 v5, v181, v185, s[8:9]
	v_cndmask_b32_e64 v6, v182, v178, s[8:9]
	v_cndmask_b32_e64 v7, v183, v179, s[8:9]
	v_cndmask_b32_e64 v8, v184, v180, s[8:9]
	v_cndmask_b32_e64 v9, v185, v181, s[8:9]
	v_add_f32_dpp v6, v2, v6 row_ror:8 row_mask:0xf bank_mask:0xf
	v_add_f32_dpp v7, v3, v7 row_ror:8 row_mask:0xf bank_mask:0xf
	v_add_f32_dpp v8, v4, v8 row_ror:8 row_mask:0xf bank_mask:0xf
	v_add_f32_dpp v9, v5, v9 row_ror:8 row_mask:0xf bank_mask:0xf
	v_cndmask_b32_e64 v2, v6, v8, s[10:11]
	v_cndmask_b32_e64 v3, v7, v9, s[10:11]
	v_cndmask_b32_e64 v4, v8, v6, s[10:11]
	v_cndmask_b32_e64 v5, v9, v7, s[10:11]
	v_add_f32_dpp v4, v2, v4 row_half_mirror row_mask:0xf bank_mask:0xf
	v_add_f32_dpp v5, v3, v5 row_half_mirror row_mask:0xf bank_mask:0xf
	v_cndmask_b32_e64 v2, v4, v5, s[14:15]
	v_cndmask_b32_e64 v3, v5, v4, s[14:15]
	s_nop 0
	v_add_f32_dpp v3, v2, v3 quad_perm:[2,3,0,1] row_mask:0xf bank_mask:0xf
	s_nop 1
	v_add_f32_dpp v11, v3, v3 quad_perm:[1,0,3,2] row_mask:0xf bank_mask:0xf
	s_mov_b64 exec, s[2:3]
	global_store_dword v[22:23], v11, off
	s_mov_b64 exec, -1
	s_waitcnt vmcnt(29)
	v_cvt_f32_ubyte0_e32 v124, v24
	v_cvt_f32_ubyte1_e32 v126, v24
	v_cvt_f32_ubyte2_e32 v128, v24
	v_cvt_f32_ubyte3_e32 v130, v24
	v_cvt_f32_ubyte0_e32 v132, v25
	v_cvt_f32_ubyte1_e32 v134, v25
	v_cvt_f32_ubyte2_e32 v136, v25
	v_cvt_f32_ubyte3_e32 v138, v25
	s_waitcnt lgkmcnt(0)
	s_load_dwordx16 s[84:99], s[36:37], 0x140 glc
	s_lshl_b32 s30, s68, 12
	s_add_u32 s28, s26, s30
	s_addc_u32 s29, s27, 0
	global_load_dwordx2 v[24:25], v162, s[28:29]
	v_cvt_f32_ubyte0_e32 v125, v26
	v_cvt_f32_ubyte1_e32 v127, v26
	v_cvt_f32_ubyte2_e32 v129, v26
	v_cvt_f32_ubyte3_e32 v131, v26
	v_cvt_f32_ubyte0_e32 v133, v27
	v_cvt_f32_ubyte1_e32 v135, v27
	v_cvt_f32_ubyte2_e32 v137, v27
	v_cvt_f32_ubyte3_e32 v139, v27
	s_lshl_b32 s30, s69, 12
	s_add_u32 s28, s26, s30
	s_addc_u32 s29, s27, 0
	global_load_dwordx2 v[26:27], v162, s[28:29]
	v_cvt_f32_ubyte0_e32 v140, v28
	v_cvt_f32_ubyte1_e32 v142, v28
	v_cvt_f32_ubyte2_e32 v144, v28
	v_cvt_f32_ubyte3_e32 v146, v28
	v_cvt_f32_ubyte0_e32 v148, v29
	v_cvt_f32_ubyte1_e32 v150, v29
	v_cvt_f32_ubyte2_e32 v152, v29
	v_cvt_f32_ubyte3_e32 v154, v29
	s_lshl_b32 s30, s70, 12
	s_add_u32 s28, s26, s30
	s_addc_u32 s29, s27, 0
	global_load_dwordx2 v[28:29], v162, s[28:29]
	v_cvt_f32_ubyte0_e32 v141, v30
	v_cvt_f32_ubyte1_e32 v143, v30
	v_cvt_f32_ubyte2_e32 v145, v30
	v_cvt_f32_ubyte3_e32 v147, v30
	v_cvt_f32_ubyte0_e32 v149, v31
	v_cvt_f32_ubyte1_e32 v151, v31
	v_cvt_f32_ubyte2_e32 v153, v31
	v_cvt_f32_ubyte3_e32 v155, v31
	s_lshl_b32 s30, s71, 12
	s_add_u32 s28, s26, s30
	s_addc_u32 s29, s27, 0
	global_load_dwordx2 v[30:31], v162, s[28:29]
	s_waitcnt vmcnt(29)
	v_cvt_f32_ubyte0_e32 v210, v32
	v_cvt_f32_ubyte1_e32 v212, v32
	v_cvt_f32_ubyte2_e32 v214, v32
	v_cvt_f32_ubyte3_e32 v216, v32
	v_cvt_f32_ubyte0_e32 v218, v33
	v_cvt_f32_ubyte1_e32 v220, v33
	v_cvt_f32_ubyte2_e32 v222, v33
	v_cvt_f32_ubyte3_e32 v224, v33
	s_lshl_b32 s30, s72, 12
	s_add_u32 s28, s26, s30
	s_addc_u32 s29, s27, 0
	global_load_dwordx2 v[32:33], v162, s[28:29]
	v_cvt_f32_ubyte0_e32 v211, v34
	v_cvt_f32_ubyte1_e32 v213, v34
	v_cvt_f32_ubyte2_e32 v215, v34
	v_cvt_f32_ubyte3_e32 v217, v34
	v_cvt_f32_ubyte0_e32 v219, v35
	v_cvt_f32_ubyte1_e32 v221, v35
	v_cvt_f32_ubyte2_e32 v223, v35
	v_cvt_f32_ubyte3_e32 v225, v35
	s_lshl_b32 s30, s73, 12
	s_add_u32 s28, s26, s30
	s_addc_u32 s29, s27, 0
	global_load_dwordx2 v[34:35], v162, s[28:29]
	v_cvt_f32_ubyte0_e32 v238, v36
	v_cvt_f32_ubyte1_e32 v240, v36
	v_cvt_f32_ubyte2_e32 v242, v36
	v_cvt_f32_ubyte3_e32 v244, v36
	v_cvt_f32_ubyte0_e32 v246, v37
	v_cvt_f32_ubyte1_e32 v248, v37
	v_cvt_f32_ubyte2_e32 v250, v37
	v_cvt_f32_ubyte3_e32 v252, v37
	s_lshl_b32 s30, s74, 12
	s_add_u32 s28, s26, s30
	s_addc_u32 s29, s27, 0
	global_load_dwordx2 v[36:37], v162, s[28:29]
	v_cvt_f32_ubyte0_e32 v239, v38
	v_cvt_f32_ubyte1_e32 v241, v38
	v_cvt_f32_ubyte2_e32 v243, v38
	v_cvt_f32_ubyte3_e32 v245, v38
	v_cvt_f32_ubyte0_e32 v247, v39
	v_cvt_f32_ubyte1_e32 v249, v39
	v_cvt_f32_ubyte2_e32 v251, v39
	v_cvt_f32_ubyte3_e32 v253, v39
	s_lshl_b32 s30, s75, 12
	s_add_u32 s28, s26, s30
	s_addc_u32 s29, s27, 0
	global_load_dwordx2 v[38:39], v162, s[28:29]
	v_mul_f32_e32 v178, v124, v108
	v_mul_f32_e32 v179, v125, v108
	v_mul_f32_e32 v180, v140, v108
	v_mul_f32_e32 v181, v141, v108
	v_mul_f32_e32 v182, v210, v108
	v_mul_f32_e32 v183, v211, v108
	v_mul_f32_e32 v184, v238, v108
	v_mul_f32_e32 v185, v239, v108
	v_fmac_f32_e32 v178, v126, v109
	v_fmac_f32_e32 v179, v127, v109
	v_fmac_f32_e32 v180, v142, v109
	v_fmac_f32_e32 v181, v143, v109
	v_fmac_f32_e32 v182, v212, v109
	v_fmac_f32_e32 v183, v213, v109
	v_fmac_f32_e32 v184, v240, v109
	v_fmac_f32_e32 v185, v241, v109
	v_fmac_f32_e32 v178, v128, v110
	v_fmac_f32_e32 v179, v129, v110
	v_fmac_f32_e32 v180, v144, v110
	v_fmac_f32_e32 v181, v145, v110
	v_fmac_f32_e32 v182, v214, v110
	v_fmac_f32_e32 v183, v215, v110
	v_fmac_f32_e32 v184, v242, v110
	v_fmac_f32_e32 v185, v243, v110
	v_fmac_f32_e32 v178, v130, v111
	v_fmac_f32_e32 v179, v131, v111
	v_fmac_f32_e32 v180, v146, v111
	v_fmac_f32_e32 v181, v147, v111
	v_fmac_f32_e32 v182, v216, v111
	v_fmac_f32_e32 v183, v217, v111
	v_fmac_f32_e32 v184, v244, v111
	v_fmac_f32_e32 v185, v245, v111
	v_fmac_f32_e32 v178, v132, v112
	v_fmac_f32_e32 v179, v133, v112
	v_fmac_f32_e32 v180, v148, v112
	v_fmac_f32_e32 v181, v149, v112
	v_fmac_f32_e32 v182, v218, v112
	v_fmac_f32_e32 v183, v219, v112
	v_fmac_f32_e32 v184, v246, v112
	v_fmac_f32_e32 v185, v247, v112
	v_fmac_f32_e32 v178, v134, v113
	v_fmac_f32_e32 v179, v135, v113
	v_fmac_f32_e32 v180, v150, v113
	v_fmac_f32_e32 v181, v151, v113
	v_fmac_f32_e32 v182, v220, v113
	v_fmac_f32_e32 v183, v221, v113
	v_fmac_f32_e32 v184, v248, v113
	v_fmac_f32_e32 v185, v249, v113
	v_fmac_f32_e32 v178, v136, v114
	v_fmac_f32_e32 v179, v137, v114
	v_fmac_f32_e32 v180, v152, v114
	v_fmac_f32_e32 v181, v153, v114
	v_fmac_f32_e32 v182, v222, v114
	v_fmac_f32_e32 v183, v223, v114
	v_fmac_f32_e32 v184, v250, v114
	v_fmac_f32_e32 v185, v251, v114
	v_fmac_f32_e32 v178, v138, v115
	v_fmac_f32_e32 v179, v139, v115
	v_fmac_f32_e32 v180, v154, v115
	v_fmac_f32_e32 v181, v155, v115
	v_fmac_f32_e32 v182, v224, v115
	v_fmac_f32_e32 v183, v225, v115
	v_fmac_f32_e32 v184, v252, v115
	v_fmac_f32_e32 v185, v253, v115
	s_waitcnt vmcnt(29)
	v_cvt_f32_ubyte0_e32 v124, v40
	v_cvt_f32_ubyte1_e32 v126, v40
	v_cvt_f32_ubyte2_e32 v128, v40
	v_cvt_f32_ubyte3_e32 v130, v40
	v_cvt_f32_ubyte0_e32 v132, v41
	v_cvt_f32_ubyte1_e32 v134, v41
	v_cvt_f32_ubyte2_e32 v136, v41
	v_cvt_f32_ubyte3_e32 v138, v41
	s_lshl_b32 s30, s76, 12
	s_add_u32 s28, s26, s30
	s_addc_u32 s29, s27, 0
	global_load_dwordx2 v[40:41], v162, s[28:29]
	v_cvt_f32_ubyte0_e32 v125, v42
	v_cvt_f32_ubyte1_e32 v127, v42
	v_cvt_f32_ubyte2_e32 v129, v42
	v_cvt_f32_ubyte3_e32 v131, v42
	v_cvt_f32_ubyte0_e32 v133, v43
	v_cvt_f32_ubyte1_e32 v135, v43
	v_cvt_f32_ubyte2_e32 v137, v43
	v_cvt_f32_ubyte3_e32 v139, v43
	s_lshl_b32 s30, s77, 12
	s_add_u32 s28, s26, s30
	s_addc_u32 s29, s27, 0
	global_load_dwordx2 v[42:43], v162, s[28:29]
	v_cvt_f32_ubyte0_e32 v140, v44
	v_cvt_f32_ubyte1_e32 v142, v44
	v_cvt_f32_ubyte2_e32 v144, v44
	v_cvt_f32_ubyte3_e32 v146, v44
	v_cvt_f32_ubyte0_e32 v148, v45
	v_cvt_f32_ubyte1_e32 v150, v45
	v_cvt_f32_ubyte2_e32 v152, v45
	v_cvt_f32_ubyte3_e32 v154, v45
	s_lshl_b32 s30, s78, 12
	s_add_u32 s28, s26, s30
	s_addc_u32 s29, s27, 0
	global_load_dwordx2 v[44:45], v162, s[28:29]
	v_cvt_f32_ubyte0_e32 v141, v46
	v_cvt_f32_ubyte1_e32 v143, v46
	v_cvt_f32_ubyte2_e32 v145, v46
	v_cvt_f32_ubyte3_e32 v147, v46
	v_cvt_f32_ubyte0_e32 v149, v47
	v_cvt_f32_ubyte1_e32 v151, v47
	v_cvt_f32_ubyte2_e32 v153, v47
	v_cvt_f32_ubyte3_e32 v155, v47
	s_lshl_b32 s30, s79, 12
	s_add_u32 s28, s26, s30
	s_addc_u32 s29, s27, 0
	global_load_dwordx2 v[46:47], v162, s[28:29]
	s_waitcnt vmcnt(29)
	v_cvt_f32_ubyte0_e32 v210, v48
	v_cvt_f32_ubyte1_e32 v212, v48
	v_cvt_f32_ubyte2_e32 v214, v48
	v_cvt_f32_ubyte3_e32 v216, v48
	v_cvt_f32_ubyte0_e32 v218, v49
	v_cvt_f32_ubyte1_e32 v220, v49
	v_cvt_f32_ubyte2_e32 v222, v49
	v_cvt_f32_ubyte3_e32 v224, v49
	s_lshl_b32 s30, s80, 12
	s_add_u32 s28, s26, s30
	s_addc_u32 s29, s27, 0
	global_load_dwordx2 v[48:49], v162, s[28:29]
	v_cvt_f32_ubyte0_e32 v211, v50
	v_cvt_f32_ubyte1_e32 v213, v50
	v_cvt_f32_ubyte2_e32 v215, v50
	v_cvt_f32_ubyte3_e32 v217, v50
	v_cvt_f32_ubyte0_e32 v219, v51
	v_cvt_f32_ubyte1_e32 v221, v51
	v_cvt_f32_ubyte2_e32 v223, v51
	v_cvt_f32_ubyte3_e32 v225, v51
	s_lshl_b32 s30, s81, 12
	s_add_u32 s28, s26, s30
	s_addc_u32 s29, s27, 0
	global_load_dwordx2 v[50:51], v162, s[28:29]
	v_cvt_f32_ubyte0_e32 v238, v52
	v_cvt_f32_ubyte1_e32 v240, v52
	v_cvt_f32_ubyte2_e32 v242, v52
	v_cvt_f32_ubyte3_e32 v244, v52
	v_cvt_f32_ubyte0_e32 v246, v53
	v_cvt_f32_ubyte1_e32 v248, v53
	v_cvt_f32_ubyte2_e32 v250, v53
	v_cvt_f32_ubyte3_e32 v252, v53
	s_lshl_b32 s30, s82, 12
	s_add_u32 s28, s26, s30
	s_addc_u32 s29, s27, 0
	global_load_dwordx2 v[52:53], v162, s[28:29]
	v_cvt_f32_ubyte0_e32 v239, v54
	v_cvt_f32_ubyte1_e32 v241, v54
	v_cvt_f32_ubyte2_e32 v243, v54
	v_cvt_f32_ubyte3_e32 v245, v54
	v_cvt_f32_ubyte0_e32 v247, v55
	v_cvt_f32_ubyte1_e32 v249, v55
	v_cvt_f32_ubyte2_e32 v251, v55
	v_cvt_f32_ubyte3_e32 v253, v55
	s_lshl_b32 s30, s83, 12
	s_add_u32 s28, s26, s30
	s_addc_u32 s29, s27, 0
	global_load_dwordx2 v[54:55], v162, s[28:29]
	v_mul_f32_e32 v186, v124, v108
	v_mul_f32_e32 v187, v125, v108
	v_mul_f32_e32 v188, v140, v108
	v_mul_f32_e32 v189, v141, v108
	v_mul_f32_e32 v190, v210, v108
	v_mul_f32_e32 v191, v211, v108
	v_mul_f32_e32 v192, v238, v108
	v_mul_f32_e32 v193, v239, v108
	v_fmac_f32_e32 v186, v126, v109
	v_fmac_f32_e32 v187, v127, v109
	v_fmac_f32_e32 v188, v142, v109
	v_fmac_f32_e32 v189, v143, v109
	v_fmac_f32_e32 v190, v212, v109
	v_fmac_f32_e32 v191, v213, v109
	v_fmac_f32_e32 v192, v240, v109
	v_fmac_f32_e32 v193, v241, v109
	v_fmac_f32_e32 v186, v128, v110
	v_fmac_f32_e32 v187, v129, v110
	v_fmac_f32_e32 v188, v144, v110
	v_fmac_f32_e32 v189, v145, v110
	v_fmac_f32_e32 v190, v214, v110
	v_fmac_f32_e32 v191, v215, v110
	v_fmac_f32_e32 v192, v242, v110
	v_fmac_f32_e32 v193, v243, v110
	v_fmac_f32_e32 v186, v130, v111
	v_fmac_f32_e32 v187, v131, v111
	v_fmac_f32_e32 v188, v146, v111
	v_fmac_f32_e32 v189, v147, v111
	v_fmac_f32_e32 v190, v216, v111
	v_fmac_f32_e32 v191, v217, v111
	v_fmac_f32_e32 v192, v244, v111
	v_fmac_f32_e32 v193, v245, v111
	v_fmac_f32_e32 v186, v132, v112
	v_fmac_f32_e32 v187, v133, v112
	v_fmac_f32_e32 v188, v148, v112
	v_fmac_f32_e32 v189, v149, v112
	v_fmac_f32_e32 v190, v218, v112
	v_fmac_f32_e32 v191, v219, v112
	v_fmac_f32_e32 v192, v246, v112
	v_fmac_f32_e32 v193, v247, v112
	v_fmac_f32_e32 v186, v134, v113
	v_fmac_f32_e32 v187, v135, v113
	v_fmac_f32_e32 v188, v150, v113
	v_fmac_f32_e32 v189, v151, v113
	v_fmac_f32_e32 v190, v220, v113
	v_fmac_f32_e32 v191, v221, v113
	v_fmac_f32_e32 v192, v248, v113
	v_fmac_f32_e32 v193, v249, v113
	v_fmac_f32_e32 v186, v136, v114
	v_fmac_f32_e32 v187, v137, v114
	v_fmac_f32_e32 v188, v152, v114
	v_fmac_f32_e32 v189, v153, v114
	v_fmac_f32_e32 v190, v222, v114
	v_fmac_f32_e32 v191, v223, v114
	v_fmac_f32_e32 v192, v250, v114
	v_fmac_f32_e32 v193, v251, v114
	v_fmac_f32_e32 v186, v138, v115
	v_fmac_f32_e32 v187, v139, v115
	v_fmac_f32_e32 v188, v154, v115
	v_fmac_f32_e32 v189, v155, v115
	v_fmac_f32_e32 v190, v224, v115
	v_fmac_f32_e32 v191, v225, v115
	v_fmac_f32_e32 v192, v252, v115
	v_fmac_f32_e32 v193, v253, v115
	s_waitcnt vmcnt(29)
	v_cvt_f32_ubyte0_e32 v124, v56
	v_cvt_f32_ubyte1_e32 v126, v56
	v_cvt_f32_ubyte2_e32 v128, v56
	v_cvt_f32_ubyte3_e32 v130, v56
	v_cvt_f32_ubyte0_e32 v132, v57
	v_cvt_f32_ubyte1_e32 v134, v57
	v_cvt_f32_ubyte2_e32 v136, v57
	v_cvt_f32_ubyte3_e32 v138, v57
	s_waitcnt lgkmcnt(0)
	s_load_dwordx16 s[68:83], s[36:37], 0x180 glc
	s_lshl_b32 s30, s84, 12
	s_add_u32 s28, s26, s30
	s_addc_u32 s29, s27, 0
	global_load_dwordx2 v[56:57], v162, s[28:29]
	v_cvt_f32_ubyte0_e32 v125, v58
	v_cvt_f32_ubyte1_e32 v127, v58
	v_cvt_f32_ubyte2_e32 v129, v58
	v_cvt_f32_ubyte3_e32 v131, v58
	v_cvt_f32_ubyte0_e32 v133, v59
	v_cvt_f32_ubyte1_e32 v135, v59
	v_cvt_f32_ubyte2_e32 v137, v59
	v_cvt_f32_ubyte3_e32 v139, v59
	s_lshl_b32 s30, s85, 12
	s_add_u32 s28, s26, s30
	s_addc_u32 s29, s27, 0
	global_load_dwordx2 v[58:59], v162, s[28:29]
	v_cvt_f32_ubyte0_e32 v140, v60
	v_cvt_f32_ubyte1_e32 v142, v60
	v_cvt_f32_ubyte2_e32 v144, v60
	v_cvt_f32_ubyte3_e32 v146, v60
	v_cvt_f32_ubyte0_e32 v148, v61
	v_cvt_f32_ubyte1_e32 v150, v61
	v_cvt_f32_ubyte2_e32 v152, v61
	v_cvt_f32_ubyte3_e32 v154, v61
	s_lshl_b32 s30, s86, 12
	s_add_u32 s28, s26, s30
	s_addc_u32 s29, s27, 0
	global_load_dwordx2 v[60:61], v162, s[28:29]
	v_cvt_f32_ubyte0_e32 v141, v62
	v_cvt_f32_ubyte1_e32 v143, v62
	v_cvt_f32_ubyte2_e32 v145, v62
	v_cvt_f32_ubyte3_e32 v147, v62
	v_cvt_f32_ubyte0_e32 v149, v63
	v_cvt_f32_ubyte1_e32 v151, v63
	v_cvt_f32_ubyte2_e32 v153, v63
	v_cvt_f32_ubyte3_e32 v155, v63
	s_lshl_b32 s30, s87, 12
	s_add_u32 s28, s26, s30
	s_addc_u32 s29, s27, 0
	global_load_dwordx2 v[62:63], v162, s[28:29]
	s_waitcnt vmcnt(29)
	v_cvt_f32_ubyte0_e32 v210, v64
	v_cvt_f32_ubyte1_e32 v212, v64
	v_cvt_f32_ubyte2_e32 v214, v64
	v_cvt_f32_ubyte3_e32 v216, v64
	v_cvt_f32_ubyte0_e32 v218, v65
	v_cvt_f32_ubyte1_e32 v220, v65
	v_cvt_f32_ubyte2_e32 v222, v65
	v_cvt_f32_ubyte3_e32 v224, v65
	s_lshl_b32 s30, s88, 12
	s_add_u32 s28, s26, s30
	s_addc_u32 s29, s27, 0
	global_load_dwordx2 v[64:65], v162, s[28:29]
	v_cvt_f32_ubyte0_e32 v211, v66
	v_cvt_f32_ubyte1_e32 v213, v66
	v_cvt_f32_ubyte2_e32 v215, v66
	v_cvt_f32_ubyte3_e32 v217, v66
	v_cvt_f32_ubyte0_e32 v219, v67
	v_cvt_f32_ubyte1_e32 v221, v67
	v_cvt_f32_ubyte2_e32 v223, v67
	v_cvt_f32_ubyte3_e32 v225, v67
	s_lshl_b32 s30, s89, 12
	s_add_u32 s28, s26, s30
	s_addc_u32 s29, s27, 0
	global_load_dwordx2 v[66:67], v162, s[28:29]
	v_cvt_f32_ubyte0_e32 v238, v68
	v_cvt_f32_ubyte1_e32 v240, v68
	v_cvt_f32_ubyte2_e32 v242, v68
	v_cvt_f32_ubyte3_e32 v244, v68
	v_cvt_f32_ubyte0_e32 v246, v69
	v_cvt_f32_ubyte1_e32 v248, v69
	v_cvt_f32_ubyte2_e32 v250, v69
	v_cvt_f32_ubyte3_e32 v252, v69
	s_lshl_b32 s30, s90, 12
	s_add_u32 s28, s26, s30
	s_addc_u32 s29, s27, 0
	global_load_dwordx2 v[68:69], v162, s[28:29]
	v_cvt_f32_ubyte0_e32 v239, v70
	v_cvt_f32_ubyte1_e32 v241, v70
	v_cvt_f32_ubyte2_e32 v243, v70
	v_cvt_f32_ubyte3_e32 v245, v70
	v_cvt_f32_ubyte0_e32 v247, v71
	v_cvt_f32_ubyte1_e32 v249, v71
	v_cvt_f32_ubyte2_e32 v251, v71
	v_cvt_f32_ubyte3_e32 v253, v71
	s_lshl_b32 s30, s91, 12
	s_add_u32 s28, s26, s30
	s_addc_u32 s29, s27, 0
	global_load_dwordx2 v[70:71], v162, s[28:29]
	v_mul_f32_e32 v194, v124, v108
	v_mul_f32_e32 v195, v125, v108
	v_mul_f32_e32 v196, v140, v108
	v_mul_f32_e32 v197, v141, v108
	v_mul_f32_e32 v198, v210, v108
	v_mul_f32_e32 v199, v211, v108
	v_mul_f32_e32 v200, v238, v108
	v_mul_f32_e32 v201, v239, v108
	v_fmac_f32_e32 v194, v126, v109
	v_fmac_f32_e32 v195, v127, v109
	v_fmac_f32_e32 v196, v142, v109
	v_fmac_f32_e32 v197, v143, v109
	v_fmac_f32_e32 v198, v212, v109
	v_fmac_f32_e32 v199, v213, v109
	v_fmac_f32_e32 v200, v240, v109
	v_fmac_f32_e32 v201, v241, v109
	v_fmac_f32_e32 v194, v128, v110
	v_fmac_f32_e32 v195, v129, v110
	v_fmac_f32_e32 v196, v144, v110
	v_fmac_f32_e32 v197, v145, v110
	v_fmac_f32_e32 v198, v214, v110
	v_fmac_f32_e32 v199, v215, v110
	v_fmac_f32_e32 v200, v242, v110
	v_fmac_f32_e32 v201, v243, v110
	v_fmac_f32_e32 v194, v130, v111
	v_fmac_f32_e32 v195, v131, v111
	v_fmac_f32_e32 v196, v146, v111
	v_fmac_f32_e32 v197, v147, v111
	v_fmac_f32_e32 v198, v216, v111
	v_fmac_f32_e32 v199, v217, v111
	v_fmac_f32_e32 v200, v244, v111
	v_fmac_f32_e32 v201, v245, v111
	v_fmac_f32_e32 v194, v132, v112
	v_fmac_f32_e32 v195, v133, v112
	v_fmac_f32_e32 v196, v148, v112
	v_fmac_f32_e32 v197, v149, v112
	v_fmac_f32_e32 v198, v218, v112
	v_fmac_f32_e32 v199, v219, v112
	v_fmac_f32_e32 v200, v246, v112
	v_fmac_f32_e32 v201, v247, v112
	v_fmac_f32_e32 v194, v134, v113
	v_fmac_f32_e32 v195, v135, v113
	v_fmac_f32_e32 v196, v150, v113
	v_fmac_f32_e32 v197, v151, v113
	v_fmac_f32_e32 v198, v220, v113
	v_fmac_f32_e32 v199, v221, v113
	v_fmac_f32_e32 v200, v248, v113
	v_fmac_f32_e32 v201, v249, v113
	v_fmac_f32_e32 v194, v136, v114
	v_fmac_f32_e32 v195, v137, v114
	v_fmac_f32_e32 v196, v152, v114
	v_fmac_f32_e32 v197, v153, v114
	v_fmac_f32_e32 v198, v222, v114
	v_fmac_f32_e32 v199, v223, v114
	v_fmac_f32_e32 v200, v250, v114
	v_fmac_f32_e32 v201, v251, v114
	v_fmac_f32_e32 v194, v138, v115
	v_fmac_f32_e32 v195, v139, v115
	v_fmac_f32_e32 v196, v154, v115
	v_fmac_f32_e32 v197, v155, v115
	v_fmac_f32_e32 v198, v224, v115
	v_fmac_f32_e32 v199, v225, v115
	v_fmac_f32_e32 v200, v252, v115
	v_fmac_f32_e32 v201, v253, v115
	s_waitcnt vmcnt(29)
	v_cvt_f32_ubyte0_e32 v124, v72
	v_cvt_f32_ubyte1_e32 v126, v72
	v_cvt_f32_ubyte2_e32 v128, v72
	v_cvt_f32_ubyte3_e32 v130, v72
	v_cvt_f32_ubyte0_e32 v132, v73
	v_cvt_f32_ubyte1_e32 v134, v73
	v_cvt_f32_ubyte2_e32 v136, v73
	v_cvt_f32_ubyte3_e32 v138, v73
	s_lshl_b32 s30, s92, 12
	s_add_u32 s28, s26, s30
	s_addc_u32 s29, s27, 0
	global_load_dwordx2 v[72:73], v162, s[28:29]
	v_cvt_f32_ubyte0_e32 v125, v74
	v_cvt_f32_ubyte1_e32 v127, v74
	v_cvt_f32_ubyte2_e32 v129, v74
	v_cvt_f32_ubyte3_e32 v131, v74
	v_cvt_f32_ubyte0_e32 v133, v75
	v_cvt_f32_ubyte1_e32 v135, v75
	v_cvt_f32_ubyte2_e32 v137, v75
	v_cvt_f32_ubyte3_e32 v139, v75
	s_lshl_b32 s30, s93, 12
	s_add_u32 s28, s26, s30
	s_addc_u32 s29, s27, 0
	global_load_dwordx2 v[74:75], v162, s[28:29]
	v_cvt_f32_ubyte0_e32 v140, v76
	v_cvt_f32_ubyte1_e32 v142, v76
	v_cvt_f32_ubyte2_e32 v144, v76
	v_cvt_f32_ubyte3_e32 v146, v76
	v_cvt_f32_ubyte0_e32 v148, v77
	v_cvt_f32_ubyte1_e32 v150, v77
	v_cvt_f32_ubyte2_e32 v152, v77
	v_cvt_f32_ubyte3_e32 v154, v77
	s_lshl_b32 s30, s94, 12
	s_add_u32 s28, s26, s30
	s_addc_u32 s29, s27, 0
	global_load_dwordx2 v[76:77], v162, s[28:29]
	v_cvt_f32_ubyte0_e32 v141, v78
	v_cvt_f32_ubyte1_e32 v143, v78
	v_cvt_f32_ubyte2_e32 v145, v78
	v_cvt_f32_ubyte3_e32 v147, v78
	v_cvt_f32_ubyte0_e32 v149, v79
	v_cvt_f32_ubyte1_e32 v151, v79
	v_cvt_f32_ubyte2_e32 v153, v79
	v_cvt_f32_ubyte3_e32 v155, v79
	s_lshl_b32 s30, s95, 12
	s_add_u32 s28, s26, s30
	s_addc_u32 s29, s27, 0
	global_load_dwordx2 v[78:79], v162, s[28:29]
	s_waitcnt vmcnt(29)
	v_cvt_f32_ubyte0_e32 v210, v80
	v_cvt_f32_ubyte1_e32 v212, v80
	v_cvt_f32_ubyte2_e32 v214, v80
	v_cvt_f32_ubyte3_e32 v216, v80
	v_cvt_f32_ubyte0_e32 v218, v81
	v_cvt_f32_ubyte1_e32 v220, v81
	v_cvt_f32_ubyte2_e32 v222, v81
	v_cvt_f32_ubyte3_e32 v224, v81
	s_lshl_b32 s30, s96, 12
	s_add_u32 s28, s26, s30
	s_addc_u32 s29, s27, 0
	global_load_dwordx2 v[80:81], v162, s[28:29]
	v_cvt_f32_ubyte0_e32 v211, v82
	v_cvt_f32_ubyte1_e32 v213, v82
	v_cvt_f32_ubyte2_e32 v215, v82
	v_cvt_f32_ubyte3_e32 v217, v82
	v_cvt_f32_ubyte0_e32 v219, v83
	v_cvt_f32_ubyte1_e32 v221, v83
	v_cvt_f32_ubyte2_e32 v223, v83
	v_cvt_f32_ubyte3_e32 v225, v83
	s_lshl_b32 s30, s97, 12
	s_add_u32 s28, s26, s30
	s_addc_u32 s29, s27, 0
	global_load_dwordx2 v[82:83], v162, s[28:29]
	v_cvt_f32_ubyte0_e32 v238, v84
	v_cvt_f32_ubyte1_e32 v240, v84
	v_cvt_f32_ubyte2_e32 v242, v84
	v_cvt_f32_ubyte3_e32 v244, v84
	v_cvt_f32_ubyte0_e32 v246, v85
	v_cvt_f32_ubyte1_e32 v248, v85
	v_cvt_f32_ubyte2_e32 v250, v85
	v_cvt_f32_ubyte3_e32 v252, v85
	s_lshl_b32 s30, s98, 12
	s_add_u32 s28, s26, s30
	s_addc_u32 s29, s27, 0
	global_load_dwordx2 v[84:85], v162, s[28:29]
	v_cvt_f32_ubyte0_e32 v239, v86
	v_cvt_f32_ubyte1_e32 v241, v86
	v_cvt_f32_ubyte2_e32 v243, v86
	v_cvt_f32_ubyte3_e32 v245, v86
	v_cvt_f32_ubyte0_e32 v247, v87
	v_cvt_f32_ubyte1_e32 v249, v87
	v_cvt_f32_ubyte2_e32 v251, v87
	v_cvt_f32_ubyte3_e32 v253, v87
	s_lshl_b32 s30, s99, 12
	s_add_u32 s28, s26, s30
	s_addc_u32 s29, s27, 0
	global_load_dwordx2 v[86:87], v162, s[28:29]
	v_mul_f32_e32 v202, v124, v108
	v_mul_f32_e32 v203, v125, v108
	v_mul_f32_e32 v204, v140, v108
	v_mul_f32_e32 v205, v141, v108
	v_mul_f32_e32 v206, v210, v108
	v_mul_f32_e32 v207, v211, v108
	v_mul_f32_e32 v208, v238, v108
	v_mul_f32_e32 v209, v239, v108
	v_fmac_f32_e32 v202, v126, v109
	v_fmac_f32_e32 v203, v127, v109
	v_fmac_f32_e32 v204, v142, v109
	v_fmac_f32_e32 v205, v143, v109
	v_fmac_f32_e32 v206, v212, v109
	v_fmac_f32_e32 v207, v213, v109
	v_fmac_f32_e32 v208, v240, v109
	v_fmac_f32_e32 v209, v241, v109
	v_fmac_f32_e32 v202, v128, v110
	v_fmac_f32_e32 v203, v129, v110
	v_fmac_f32_e32 v204, v144, v110
	v_fmac_f32_e32 v205, v145, v110
	v_fmac_f32_e32 v206, v214, v110
	v_fmac_f32_e32 v207, v215, v110
	v_fmac_f32_e32 v208, v242, v110
	v_fmac_f32_e32 v209, v243, v110
	v_fmac_f32_e32 v202, v130, v111
	v_fmac_f32_e32 v203, v131, v111
	v_fmac_f32_e32 v204, v146, v111
	v_fmac_f32_e32 v205, v147, v111
	v_fmac_f32_e32 v206, v216, v111
	v_fmac_f32_e32 v207, v217, v111
	v_fmac_f32_e32 v208, v244, v111
	v_fmac_f32_e32 v209, v245, v111
	v_fmac_f32_e32 v202, v132, v112
	v_fmac_f32_e32 v203, v133, v112
	v_fmac_f32_e32 v204, v148, v112
	v_fmac_f32_e32 v205, v149, v112
	v_fmac_f32_e32 v206, v218, v112
	v_fmac_f32_e32 v207, v219, v112
	v_fmac_f32_e32 v208, v246, v112
	v_fmac_f32_e32 v209, v247, v112
	v_fmac_f32_e32 v202, v134, v113
	v_fmac_f32_e32 v203, v135, v113
	v_fmac_f32_e32 v204, v150, v113
	v_fmac_f32_e32 v205, v151, v113
	v_fmac_f32_e32 v206, v220, v113
	v_fmac_f32_e32 v207, v221, v113
	v_fmac_f32_e32 v208, v248, v113
	v_fmac_f32_e32 v209, v249, v113
	v_fmac_f32_e32 v202, v136, v114
	v_fmac_f32_e32 v203, v137, v114
	v_fmac_f32_e32 v204, v152, v114
	v_fmac_f32_e32 v205, v153, v114
	v_fmac_f32_e32 v206, v222, v114
	v_fmac_f32_e32 v207, v223, v114
	v_fmac_f32_e32 v208, v250, v114
	v_fmac_f32_e32 v209, v251, v114
	v_fmac_f32_e32 v202, v138, v115
	v_fmac_f32_e32 v203, v139, v115
	v_fmac_f32_e32 v204, v154, v115
	v_fmac_f32_e32 v205, v155, v115
	v_fmac_f32_e32 v206, v224, v115
	v_fmac_f32_e32 v207, v225, v115
	v_fmac_f32_e32 v208, v252, v115
	v_fmac_f32_e32 v209, v253, v115
	v_permlane32_swap_b32_e32 v178, v194
	v_permlane32_swap_b32_e32 v179, v195
	v_permlane32_swap_b32_e32 v180, v196
	v_permlane32_swap_b32_e32 v181, v197
	v_permlane32_swap_b32_e32 v182, v198
	v_permlane32_swap_b32_e32 v183, v199
	v_permlane32_swap_b32_e32 v184, v200
	v_permlane32_swap_b32_e32 v185, v201
	v_permlane32_swap_b32_e32 v186, v202
	v_permlane32_swap_b32_e32 v187, v203
	v_permlane32_swap_b32_e32 v188, v204
	v_permlane32_swap_b32_e32 v189, v205
	v_permlane32_swap_b32_e32 v190, v206
	v_permlane32_swap_b32_e32 v191, v207
	v_permlane32_swap_b32_e32 v192, v208
	v_permlane32_swap_b32_e32 v193, v209
	v_add_f32_e32 v178, v178, v194
	v_add_f32_e32 v179, v179, v195
	v_add_f32_e32 v180, v180, v196
	v_add_f32_e32 v181, v181, v197
	v_add_f32_e32 v182, v182, v198
	v_add_f32_e32 v183, v183, v199
	v_add_f32_e32 v184, v184, v200
	v_add_f32_e32 v185, v185, v201
	v_add_f32_e32 v186, v186, v202
	v_add_f32_e32 v187, v187, v203
	v_add_f32_e32 v188, v188, v204
	v_add_f32_e32 v189, v189, v205
	v_add_f32_e32 v190, v190, v206
	v_add_f32_e32 v191, v191, v207
	v_add_f32_e32 v192, v192, v208
	v_add_f32_e32 v193, v193, v209
	v_permlane16_swap_b32_e32 v178, v186
	v_permlane16_swap_b32_e32 v179, v187
	v_permlane16_swap_b32_e32 v180, v188
	v_permlane16_swap_b32_e32 v181, v189
	v_permlane16_swap_b32_e32 v182, v190
	v_permlane16_swap_b32_e32 v183, v191
	v_permlane16_swap_b32_e32 v184, v192
	v_permlane16_swap_b32_e32 v185, v193
	v_add_f32_e32 v178, v178, v186
	v_add_f32_e32 v179, v179, v187
	v_add_f32_e32 v180, v180, v188
	v_add_f32_e32 v181, v181, v189
	v_add_f32_e32 v182, v182, v190
	v_add_f32_e32 v183, v183, v191
	v_add_f32_e32 v184, v184, v192
	v_add_f32_e32 v185, v185, v193
	v_cndmask_b32_e64 v2, v178, v182, s[8:9]
	v_cndmask_b32_e64 v3, v179, v183, s[8:9]
	v_cndmask_b32_e64 v4, v180, v184, s[8:9]
	v_cndmask_b32_e64 v5, v181, v185, s[8:9]
	v_cndmask_b32_e64 v6, v182, v178, s[8:9]
	v_cndmask_b32_e64 v7, v183, v179, s[8:9]
	v_cndmask_b32_e64 v8, v184, v180, s[8:9]
	v_cndmask_b32_e64 v9, v185, v181, s[8:9]
	v_add_f32_dpp v6, v2, v6 row_ror:8 row_mask:0xf bank_mask:0xf
	v_add_f32_dpp v7, v3, v7 row_ror:8 row_mask:0xf bank_mask:0xf
	v_add_f32_dpp v8, v4, v8 row_ror:8 row_mask:0xf bank_mask:0xf
	v_add_f32_dpp v9, v5, v9 row_ror:8 row_mask:0xf bank_mask:0xf
	v_cndmask_b32_e64 v2, v6, v8, s[10:11]
	v_cndmask_b32_e64 v3, v7, v9, s[10:11]
	v_cndmask_b32_e64 v4, v8, v6, s[10:11]
	v_cndmask_b32_e64 v5, v9, v7, s[10:11]
	v_add_f32_dpp v4, v2, v4 row_half_mirror row_mask:0xf bank_mask:0xf
	v_add_f32_dpp v5, v3, v5 row_half_mirror row_mask:0xf bank_mask:0xf
	v_cndmask_b32_e64 v2, v4, v5, s[14:15]
	v_cndmask_b32_e64 v3, v5, v4, s[14:15]
	s_nop 0
	v_add_f32_dpp v3, v2, v3 quad_perm:[2,3,0,1] row_mask:0xf bank_mask:0xf
	s_nop 1
	v_add_f32_dpp v11, v3, v3 quad_perm:[1,0,3,2] row_mask:0xf bank_mask:0xf
	s_mov_b64 exec, s[2:3]
	global_store_dword v[22:23], v11, off offset:128
	s_mov_b64 exec, -1
	s_waitcnt vmcnt(29)
	v_cvt_f32_ubyte0_e32 v124, v24
	v_cvt_f32_ubyte1_e32 v126, v24
	v_cvt_f32_ubyte2_e32 v128, v24
	v_cvt_f32_ubyte3_e32 v130, v24
	v_cvt_f32_ubyte0_e32 v132, v25
	v_cvt_f32_ubyte1_e32 v134, v25
	v_cvt_f32_ubyte2_e32 v136, v25
	v_cvt_f32_ubyte3_e32 v138, v25
	s_waitcnt lgkmcnt(0)
	s_load_dwordx16 s[84:99], s[36:37], 0x1c0 glc
	s_lshl_b32 s30, s68, 12
	s_add_u32 s28, s26, s30
	s_addc_u32 s29, s27, 0
	global_load_dwordx2 v[24:25], v162, s[28:29]
	v_cvt_f32_ubyte0_e32 v125, v26
	v_cvt_f32_ubyte1_e32 v127, v26
	v_cvt_f32_ubyte2_e32 v129, v26
	v_cvt_f32_ubyte3_e32 v131, v26
	v_cvt_f32_ubyte0_e32 v133, v27
	v_cvt_f32_ubyte1_e32 v135, v27
	v_cvt_f32_ubyte2_e32 v137, v27
	v_cvt_f32_ubyte3_e32 v139, v27
	s_lshl_b32 s30, s69, 12
	s_add_u32 s28, s26, s30
	s_addc_u32 s29, s27, 0
	global_load_dwordx2 v[26:27], v162, s[28:29]
	v_cvt_f32_ubyte0_e32 v140, v28
	v_cvt_f32_ubyte1_e32 v142, v28
	v_cvt_f32_ubyte2_e32 v144, v28
	v_cvt_f32_ubyte3_e32 v146, v28
	v_cvt_f32_ubyte0_e32 v148, v29
	v_cvt_f32_ubyte1_e32 v150, v29
	v_cvt_f32_ubyte2_e32 v152, v29
	v_cvt_f32_ubyte3_e32 v154, v29
	s_lshl_b32 s30, s70, 12
	s_add_u32 s28, s26, s30
	s_addc_u32 s29, s27, 0
	global_load_dwordx2 v[28:29], v162, s[28:29]
	v_cvt_f32_ubyte0_e32 v141, v30
	v_cvt_f32_ubyte1_e32 v143, v30
	v_cvt_f32_ubyte2_e32 v145, v30
	v_cvt_f32_ubyte3_e32 v147, v30
	v_cvt_f32_ubyte0_e32 v149, v31
	v_cvt_f32_ubyte1_e32 v151, v31
	v_cvt_f32_ubyte2_e32 v153, v31
	v_cvt_f32_ubyte3_e32 v155, v31
	s_lshl_b32 s30, s71, 12
	s_add_u32 s28, s26, s30
	s_addc_u32 s29, s27, 0
	global_load_dwordx2 v[30:31], v162, s[28:29]
	s_waitcnt vmcnt(29)
	v_cvt_f32_ubyte0_e32 v210, v32
	v_cvt_f32_ubyte1_e32 v212, v32
	v_cvt_f32_ubyte2_e32 v214, v32
	v_cvt_f32_ubyte3_e32 v216, v32
	v_cvt_f32_ubyte0_e32 v218, v33
	v_cvt_f32_ubyte1_e32 v220, v33
	v_cvt_f32_ubyte2_e32 v222, v33
	v_cvt_f32_ubyte3_e32 v224, v33
	s_lshl_b32 s30, s72, 12
	s_add_u32 s28, s26, s30
	s_addc_u32 s29, s27, 0
	global_load_dwordx2 v[32:33], v162, s[28:29]
	v_cvt_f32_ubyte0_e32 v211, v34
	v_cvt_f32_ubyte1_e32 v213, v34
	v_cvt_f32_ubyte2_e32 v215, v34
	v_cvt_f32_ubyte3_e32 v217, v34
	v_cvt_f32_ubyte0_e32 v219, v35
	v_cvt_f32_ubyte1_e32 v221, v35
	v_cvt_f32_ubyte2_e32 v223, v35
	v_cvt_f32_ubyte3_e32 v225, v35
	s_lshl_b32 s30, s73, 12
	s_add_u32 s28, s26, s30
	s_addc_u32 s29, s27, 0
	global_load_dwordx2 v[34:35], v162, s[28:29]
	v_cvt_f32_ubyte0_e32 v238, v36
	v_cvt_f32_ubyte1_e32 v240, v36
	v_cvt_f32_ubyte2_e32 v242, v36
	v_cvt_f32_ubyte3_e32 v244, v36
	v_cvt_f32_ubyte0_e32 v246, v37
	v_cvt_f32_ubyte1_e32 v248, v37
	v_cvt_f32_ubyte2_e32 v250, v37
	v_cvt_f32_ubyte3_e32 v252, v37
	s_lshl_b32 s30, s74, 12
	s_add_u32 s28, s26, s30
	s_addc_u32 s29, s27, 0
	global_load_dwordx2 v[36:37], v162, s[28:29]
	v_cvt_f32_ubyte0_e32 v239, v38
	v_cvt_f32_ubyte1_e32 v241, v38
	v_cvt_f32_ubyte2_e32 v243, v38
	v_cvt_f32_ubyte3_e32 v245, v38
	v_cvt_f32_ubyte0_e32 v247, v39
	v_cvt_f32_ubyte1_e32 v249, v39
	v_cvt_f32_ubyte2_e32 v251, v39
	v_cvt_f32_ubyte3_e32 v253, v39
	s_lshl_b32 s30, s75, 12
	s_add_u32 s28, s26, s30
	s_addc_u32 s29, s27, 0
	global_load_dwordx2 v[38:39], v162, s[28:29]
	v_mul_f32_e32 v178, v124, v108
	v_mul_f32_e32 v179, v125, v108
	v_mul_f32_e32 v180, v140, v108
	v_mul_f32_e32 v181, v141, v108
	v_mul_f32_e32 v182, v210, v108
	v_mul_f32_e32 v183, v211, v108
	v_mul_f32_e32 v184, v238, v108
	v_mul_f32_e32 v185, v239, v108
	v_fmac_f32_e32 v178, v126, v109
	v_fmac_f32_e32 v179, v127, v109
	v_fmac_f32_e32 v180, v142, v109
	v_fmac_f32_e32 v181, v143, v109
	v_fmac_f32_e32 v182, v212, v109
	v_fmac_f32_e32 v183, v213, v109
	v_fmac_f32_e32 v184, v240, v109
	v_fmac_f32_e32 v185, v241, v109
	v_fmac_f32_e32 v178, v128, v110
	v_fmac_f32_e32 v179, v129, v110
	v_fmac_f32_e32 v180, v144, v110
	v_fmac_f32_e32 v181, v145, v110
	v_fmac_f32_e32 v182, v214, v110
	v_fmac_f32_e32 v183, v215, v110
	v_fmac_f32_e32 v184, v242, v110
	v_fmac_f32_e32 v185, v243, v110
	v_fmac_f32_e32 v178, v130, v111
	v_fmac_f32_e32 v179, v131, v111
	v_fmac_f32_e32 v180, v146, v111
	v_fmac_f32_e32 v181, v147, v111
	v_fmac_f32_e32 v182, v216, v111
	v_fmac_f32_e32 v183, v217, v111
	v_fmac_f32_e32 v184, v244, v111
	v_fmac_f32_e32 v185, v245, v111
	v_fmac_f32_e32 v178, v132, v112
	v_fmac_f32_e32 v179, v133, v112
	v_fmac_f32_e32 v180, v148, v112
	v_fmac_f32_e32 v181, v149, v112
	v_fmac_f32_e32 v182, v218, v112
	v_fmac_f32_e32 v183, v219, v112
	v_fmac_f32_e32 v184, v246, v112
	v_fmac_f32_e32 v185, v247, v112
	v_fmac_f32_e32 v178, v134, v113
	v_fmac_f32_e32 v179, v135, v113
	v_fmac_f32_e32 v180, v150, v113
	v_fmac_f32_e32 v181, v151, v113
	v_fmac_f32_e32 v182, v220, v113
	v_fmac_f32_e32 v183, v221, v113
	v_fmac_f32_e32 v184, v248, v113
	v_fmac_f32_e32 v185, v249, v113
	v_fmac_f32_e32 v178, v136, v114
	v_fmac_f32_e32 v179, v137, v114
	v_fmac_f32_e32 v180, v152, v114
	v_fmac_f32_e32 v181, v153, v114
	v_fmac_f32_e32 v182, v222, v114
	v_fmac_f32_e32 v183, v223, v114
	v_fmac_f32_e32 v184, v250, v114
	v_fmac_f32_e32 v185, v251, v114
	v_fmac_f32_e32 v178, v138, v115
	v_fmac_f32_e32 v179, v139, v115
	v_fmac_f32_e32 v180, v154, v115
	v_fmac_f32_e32 v181, v155, v115
	v_fmac_f32_e32 v182, v224, v115
	v_fmac_f32_e32 v183, v225, v115
	v_fmac_f32_e32 v184, v252, v115
	v_fmac_f32_e32 v185, v253, v115
	s_waitcnt vmcnt(29)
	v_cvt_f32_ubyte0_e32 v124, v40
	v_cvt_f32_ubyte1_e32 v126, v40
	v_cvt_f32_ubyte2_e32 v128, v40
	v_cvt_f32_ubyte3_e32 v130, v40
	v_cvt_f32_ubyte0_e32 v132, v41
	v_cvt_f32_ubyte1_e32 v134, v41
	v_cvt_f32_ubyte2_e32 v136, v41
	v_cvt_f32_ubyte3_e32 v138, v41
	s_lshl_b32 s30, s76, 12
	s_add_u32 s28, s26, s30
	s_addc_u32 s29, s27, 0
	global_load_dwordx2 v[40:41], v162, s[28:29]
	v_cvt_f32_ubyte0_e32 v125, v42
	v_cvt_f32_ubyte1_e32 v127, v42
	v_cvt_f32_ubyte2_e32 v129, v42
	v_cvt_f32_ubyte3_e32 v131, v42
	v_cvt_f32_ubyte0_e32 v133, v43
	v_cvt_f32_ubyte1_e32 v135, v43
	v_cvt_f32_ubyte2_e32 v137, v43
	v_cvt_f32_ubyte3_e32 v139, v43
	s_lshl_b32 s30, s77, 12
	s_add_u32 s28, s26, s30
	s_addc_u32 s29, s27, 0
	global_load_dwordx2 v[42:43], v162, s[28:29]
	v_cvt_f32_ubyte0_e32 v140, v44
	v_cvt_f32_ubyte1_e32 v142, v44
	v_cvt_f32_ubyte2_e32 v144, v44
	v_cvt_f32_ubyte3_e32 v146, v44
	v_cvt_f32_ubyte0_e32 v148, v45
	v_cvt_f32_ubyte1_e32 v150, v45
	v_cvt_f32_ubyte2_e32 v152, v45
	v_cvt_f32_ubyte3_e32 v154, v45
	s_lshl_b32 s30, s78, 12
	s_add_u32 s28, s26, s30
	s_addc_u32 s29, s27, 0
	global_load_dwordx2 v[44:45], v162, s[28:29]
	v_cvt_f32_ubyte0_e32 v141, v46
	v_cvt_f32_ubyte1_e32 v143, v46
	v_cvt_f32_ubyte2_e32 v145, v46
	v_cvt_f32_ubyte3_e32 v147, v46
	v_cvt_f32_ubyte0_e32 v149, v47
	v_cvt_f32_ubyte1_e32 v151, v47
	v_cvt_f32_ubyte2_e32 v153, v47
	v_cvt_f32_ubyte3_e32 v155, v47
	s_lshl_b32 s30, s79, 12
	s_add_u32 s28, s26, s30
	s_addc_u32 s29, s27, 0
	global_load_dwordx2 v[46:47], v162, s[28:29]
	s_waitcnt vmcnt(29)
	v_cvt_f32_ubyte0_e32 v210, v48
	v_cvt_f32_ubyte1_e32 v212, v48
	v_cvt_f32_ubyte2_e32 v214, v48
	v_cvt_f32_ubyte3_e32 v216, v48
	v_cvt_f32_ubyte0_e32 v218, v49
	v_cvt_f32_ubyte1_e32 v220, v49
	v_cvt_f32_ubyte2_e32 v222, v49
	v_cvt_f32_ubyte3_e32 v224, v49
	s_lshl_b32 s30, s80, 12
	s_add_u32 s28, s26, s30
	s_addc_u32 s29, s27, 0
	global_load_dwordx2 v[48:49], v162, s[28:29]
	v_cvt_f32_ubyte0_e32 v211, v50
	v_cvt_f32_ubyte1_e32 v213, v50
	v_cvt_f32_ubyte2_e32 v215, v50
	v_cvt_f32_ubyte3_e32 v217, v50
	v_cvt_f32_ubyte0_e32 v219, v51
	v_cvt_f32_ubyte1_e32 v221, v51
	v_cvt_f32_ubyte2_e32 v223, v51
	v_cvt_f32_ubyte3_e32 v225, v51
	s_lshl_b32 s30, s81, 12
	s_add_u32 s28, s26, s30
	s_addc_u32 s29, s27, 0
	global_load_dwordx2 v[50:51], v162, s[28:29]
	v_cvt_f32_ubyte0_e32 v238, v52
	v_cvt_f32_ubyte1_e32 v240, v52
	v_cvt_f32_ubyte2_e32 v242, v52
	v_cvt_f32_ubyte3_e32 v244, v52
	v_cvt_f32_ubyte0_e32 v246, v53
	v_cvt_f32_ubyte1_e32 v248, v53
	v_cvt_f32_ubyte2_e32 v250, v53
	v_cvt_f32_ubyte3_e32 v252, v53
	s_lshl_b32 s30, s82, 12
	s_add_u32 s28, s26, s30
	s_addc_u32 s29, s27, 0
	global_load_dwordx2 v[52:53], v162, s[28:29]
	v_cvt_f32_ubyte0_e32 v239, v54
	v_cvt_f32_ubyte1_e32 v241, v54
	v_cvt_f32_ubyte2_e32 v243, v54
	v_cvt_f32_ubyte3_e32 v245, v54
	v_cvt_f32_ubyte0_e32 v247, v55
	v_cvt_f32_ubyte1_e32 v249, v55
	v_cvt_f32_ubyte2_e32 v251, v55
	v_cvt_f32_ubyte3_e32 v253, v55
	s_lshl_b32 s30, s83, 12
	s_add_u32 s28, s26, s30
	s_addc_u32 s29, s27, 0
	global_load_dwordx2 v[54:55], v162, s[28:29]
	v_mul_f32_e32 v186, v124, v108
	v_mul_f32_e32 v187, v125, v108
	v_mul_f32_e32 v188, v140, v108
	v_mul_f32_e32 v189, v141, v108
	v_mul_f32_e32 v190, v210, v108
	v_mul_f32_e32 v191, v211, v108
	v_mul_f32_e32 v192, v238, v108
	v_mul_f32_e32 v193, v239, v108
	v_fmac_f32_e32 v186, v126, v109
	v_fmac_f32_e32 v187, v127, v109
	v_fmac_f32_e32 v188, v142, v109
	v_fmac_f32_e32 v189, v143, v109
	v_fmac_f32_e32 v190, v212, v109
	v_fmac_f32_e32 v191, v213, v109
	v_fmac_f32_e32 v192, v240, v109
	v_fmac_f32_e32 v193, v241, v109
	v_fmac_f32_e32 v186, v128, v110
	v_fmac_f32_e32 v187, v129, v110
	v_fmac_f32_e32 v188, v144, v110
	v_fmac_f32_e32 v189, v145, v110
	v_fmac_f32_e32 v190, v214, v110
	v_fmac_f32_e32 v191, v215, v110
	v_fmac_f32_e32 v192, v242, v110
	v_fmac_f32_e32 v193, v243, v110
	v_fmac_f32_e32 v186, v130, v111
	v_fmac_f32_e32 v187, v131, v111
	v_fmac_f32_e32 v188, v146, v111
	v_fmac_f32_e32 v189, v147, v111
	v_fmac_f32_e32 v190, v216, v111
	v_fmac_f32_e32 v191, v217, v111
	v_fmac_f32_e32 v192, v244, v111
	v_fmac_f32_e32 v193, v245, v111
	v_fmac_f32_e32 v186, v132, v112
	v_fmac_f32_e32 v187, v133, v112
	v_fmac_f32_e32 v188, v148, v112
	v_fmac_f32_e32 v189, v149, v112
	v_fmac_f32_e32 v190, v218, v112
	v_fmac_f32_e32 v191, v219, v112
	v_fmac_f32_e32 v192, v246, v112
	v_fmac_f32_e32 v193, v247, v112
	v_fmac_f32_e32 v186, v134, v113
	v_fmac_f32_e32 v187, v135, v113
	v_fmac_f32_e32 v188, v150, v113
	v_fmac_f32_e32 v189, v151, v113
	v_fmac_f32_e32 v190, v220, v113
	v_fmac_f32_e32 v191, v221, v113
	v_fmac_f32_e32 v192, v248, v113
	v_fmac_f32_e32 v193, v249, v113
	v_fmac_f32_e32 v186, v136, v114
	v_fmac_f32_e32 v187, v137, v114
	v_fmac_f32_e32 v188, v152, v114
	v_fmac_f32_e32 v189, v153, v114
	v_fmac_f32_e32 v190, v222, v114
	v_fmac_f32_e32 v191, v223, v114
	v_fmac_f32_e32 v192, v250, v114
	v_fmac_f32_e32 v193, v251, v114
	v_fmac_f32_e32 v186, v138, v115
	v_fmac_f32_e32 v187, v139, v115
	v_fmac_f32_e32 v188, v154, v115
	v_fmac_f32_e32 v189, v155, v115
	v_fmac_f32_e32 v190, v224, v115
	v_fmac_f32_e32 v191, v225, v115
	v_fmac_f32_e32 v192, v252, v115
	v_fmac_f32_e32 v193, v253, v115
	s_waitcnt vmcnt(29)
	v_cvt_f32_ubyte0_e32 v124, v56
	v_cvt_f32_ubyte1_e32 v126, v56
	v_cvt_f32_ubyte2_e32 v128, v56
	v_cvt_f32_ubyte3_e32 v130, v56
	v_cvt_f32_ubyte0_e32 v132, v57
	v_cvt_f32_ubyte1_e32 v134, v57
	v_cvt_f32_ubyte2_e32 v136, v57
	v_cvt_f32_ubyte3_e32 v138, v57
	s_waitcnt lgkmcnt(0)
	s_load_dwordx16 s[68:83], s[38:39], 0x0 glc
	s_lshl_b32 s30, s84, 12
	s_add_u32 s28, s26, s30
	s_addc_u32 s29, s27, 0
	global_load_dwordx2 v[56:57], v162, s[28:29]
	v_cvt_f32_ubyte0_e32 v125, v58
	v_cvt_f32_ubyte1_e32 v127, v58
	v_cvt_f32_ubyte2_e32 v129, v58
	v_cvt_f32_ubyte3_e32 v131, v58
	v_cvt_f32_ubyte0_e32 v133, v59
	v_cvt_f32_ubyte1_e32 v135, v59
	v_cvt_f32_ubyte2_e32 v137, v59
	v_cvt_f32_ubyte3_e32 v139, v59
	s_lshl_b32 s30, s85, 12
	s_add_u32 s28, s26, s30
	s_addc_u32 s29, s27, 0
	global_load_dwordx2 v[58:59], v162, s[28:29]
	v_cvt_f32_ubyte0_e32 v140, v60
	v_cvt_f32_ubyte1_e32 v142, v60
	v_cvt_f32_ubyte2_e32 v144, v60
	v_cvt_f32_ubyte3_e32 v146, v60
	v_cvt_f32_ubyte0_e32 v148, v61
	v_cvt_f32_ubyte1_e32 v150, v61
	v_cvt_f32_ubyte2_e32 v152, v61
	v_cvt_f32_ubyte3_e32 v154, v61
	s_lshl_b32 s30, s86, 12
	s_add_u32 s28, s26, s30
	s_addc_u32 s29, s27, 0
	global_load_dwordx2 v[60:61], v162, s[28:29]
	v_cvt_f32_ubyte0_e32 v141, v62
	v_cvt_f32_ubyte1_e32 v143, v62
	v_cvt_f32_ubyte2_e32 v145, v62
	v_cvt_f32_ubyte3_e32 v147, v62
	v_cvt_f32_ubyte0_e32 v149, v63
	v_cvt_f32_ubyte1_e32 v151, v63
	v_cvt_f32_ubyte2_e32 v153, v63
	v_cvt_f32_ubyte3_e32 v155, v63
	s_lshl_b32 s30, s87, 12
	s_add_u32 s28, s26, s30
	s_addc_u32 s29, s27, 0
	global_load_dwordx2 v[62:63], v162, s[28:29]
	s_waitcnt vmcnt(29)
	v_cvt_f32_ubyte0_e32 v210, v64
	v_cvt_f32_ubyte1_e32 v212, v64
	v_cvt_f32_ubyte2_e32 v214, v64
	v_cvt_f32_ubyte3_e32 v216, v64
	v_cvt_f32_ubyte0_e32 v218, v65
	v_cvt_f32_ubyte1_e32 v220, v65
	v_cvt_f32_ubyte2_e32 v222, v65
	v_cvt_f32_ubyte3_e32 v224, v65
	s_lshl_b32 s30, s88, 12
	s_add_u32 s28, s26, s30
	s_addc_u32 s29, s27, 0
	global_load_dwordx2 v[64:65], v162, s[28:29]
	v_cvt_f32_ubyte0_e32 v211, v66
	v_cvt_f32_ubyte1_e32 v213, v66
	v_cvt_f32_ubyte2_e32 v215, v66
	v_cvt_f32_ubyte3_e32 v217, v66
	v_cvt_f32_ubyte0_e32 v219, v67
	v_cvt_f32_ubyte1_e32 v221, v67
	v_cvt_f32_ubyte2_e32 v223, v67
	v_cvt_f32_ubyte3_e32 v225, v67
	s_lshl_b32 s30, s89, 12
	s_add_u32 s28, s26, s30
	s_addc_u32 s29, s27, 0
	global_load_dwordx2 v[66:67], v162, s[28:29]
	v_cvt_f32_ubyte0_e32 v238, v68
	v_cvt_f32_ubyte1_e32 v240, v68
	v_cvt_f32_ubyte2_e32 v242, v68
	v_cvt_f32_ubyte3_e32 v244, v68
	v_cvt_f32_ubyte0_e32 v246, v69
	v_cvt_f32_ubyte1_e32 v248, v69
	v_cvt_f32_ubyte2_e32 v250, v69
	v_cvt_f32_ubyte3_e32 v252, v69
	s_lshl_b32 s30, s90, 12
	s_add_u32 s28, s26, s30
	s_addc_u32 s29, s27, 0
	global_load_dwordx2 v[68:69], v162, s[28:29]
	v_cvt_f32_ubyte0_e32 v239, v70
	v_cvt_f32_ubyte1_e32 v241, v70
	v_cvt_f32_ubyte2_e32 v243, v70
	v_cvt_f32_ubyte3_e32 v245, v70
	v_cvt_f32_ubyte0_e32 v247, v71
	v_cvt_f32_ubyte1_e32 v249, v71
	v_cvt_f32_ubyte2_e32 v251, v71
	v_cvt_f32_ubyte3_e32 v253, v71
	s_lshl_b32 s30, s91, 12
	s_add_u32 s28, s26, s30
	s_addc_u32 s29, s27, 0
	global_load_dwordx2 v[70:71], v162, s[28:29]
	v_mul_f32_e32 v194, v124, v108
	v_mul_f32_e32 v195, v125, v108
	v_mul_f32_e32 v196, v140, v108
	v_mul_f32_e32 v197, v141, v108
	v_mul_f32_e32 v198, v210, v108
	v_mul_f32_e32 v199, v211, v108
	v_mul_f32_e32 v200, v238, v108
	v_mul_f32_e32 v201, v239, v108
	v_fmac_f32_e32 v194, v126, v109
	v_fmac_f32_e32 v195, v127, v109
	v_fmac_f32_e32 v196, v142, v109
	v_fmac_f32_e32 v197, v143, v109
	v_fmac_f32_e32 v198, v212, v109
	v_fmac_f32_e32 v199, v213, v109
	v_fmac_f32_e32 v200, v240, v109
	v_fmac_f32_e32 v201, v241, v109
	v_fmac_f32_e32 v194, v128, v110
	v_fmac_f32_e32 v195, v129, v110
	v_fmac_f32_e32 v196, v144, v110
	v_fmac_f32_e32 v197, v145, v110
	v_fmac_f32_e32 v198, v214, v110
	v_fmac_f32_e32 v199, v215, v110
	v_fmac_f32_e32 v200, v242, v110
	v_fmac_f32_e32 v201, v243, v110
	v_fmac_f32_e32 v194, v130, v111
	v_fmac_f32_e32 v195, v131, v111
	v_fmac_f32_e32 v196, v146, v111
	v_fmac_f32_e32 v197, v147, v111
	v_fmac_f32_e32 v198, v216, v111
	v_fmac_f32_e32 v199, v217, v111
	v_fmac_f32_e32 v200, v244, v111
	v_fmac_f32_e32 v201, v245, v111
	v_fmac_f32_e32 v194, v132, v112
	v_fmac_f32_e32 v195, v133, v112
	v_fmac_f32_e32 v196, v148, v112
	v_fmac_f32_e32 v197, v149, v112
	v_fmac_f32_e32 v198, v218, v112
	v_fmac_f32_e32 v199, v219, v112
	v_fmac_f32_e32 v200, v246, v112
	v_fmac_f32_e32 v201, v247, v112
	v_fmac_f32_e32 v194, v134, v113
	v_fmac_f32_e32 v195, v135, v113
	v_fmac_f32_e32 v196, v150, v113
	v_fmac_f32_e32 v197, v151, v113
	v_fmac_f32_e32 v198, v220, v113
	v_fmac_f32_e32 v199, v221, v113
	v_fmac_f32_e32 v200, v248, v113
	v_fmac_f32_e32 v201, v249, v113
	v_fmac_f32_e32 v194, v136, v114
	v_fmac_f32_e32 v195, v137, v114
	v_fmac_f32_e32 v196, v152, v114
	v_fmac_f32_e32 v197, v153, v114
	v_fmac_f32_e32 v198, v222, v114
	v_fmac_f32_e32 v199, v223, v114
	v_fmac_f32_e32 v200, v250, v114
	v_fmac_f32_e32 v201, v251, v114
	v_fmac_f32_e32 v194, v138, v115
	v_fmac_f32_e32 v195, v139, v115
	v_fmac_f32_e32 v196, v154, v115
	v_fmac_f32_e32 v197, v155, v115
	v_fmac_f32_e32 v198, v224, v115
	v_fmac_f32_e32 v199, v225, v115
	v_fmac_f32_e32 v200, v252, v115
	v_fmac_f32_e32 v201, v253, v115
	s_waitcnt vmcnt(29)
	v_cvt_f32_ubyte0_e32 v124, v72
	v_cvt_f32_ubyte1_e32 v126, v72
	v_cvt_f32_ubyte2_e32 v128, v72
	v_cvt_f32_ubyte3_e32 v130, v72
	v_cvt_f32_ubyte0_e32 v132, v73
	v_cvt_f32_ubyte1_e32 v134, v73
	v_cvt_f32_ubyte2_e32 v136, v73
	v_cvt_f32_ubyte3_e32 v138, v73
	s_lshl_b32 s30, s92, 12
	s_add_u32 s28, s26, s30
	s_addc_u32 s29, s27, 0
	global_load_dwordx2 v[72:73], v162, s[28:29]
	v_cvt_f32_ubyte0_e32 v125, v74
	v_cvt_f32_ubyte1_e32 v127, v74
	v_cvt_f32_ubyte2_e32 v129, v74
	v_cvt_f32_ubyte3_e32 v131, v74
	v_cvt_f32_ubyte0_e32 v133, v75
	v_cvt_f32_ubyte1_e32 v135, v75
	v_cvt_f32_ubyte2_e32 v137, v75
	v_cvt_f32_ubyte3_e32 v139, v75
	s_lshl_b32 s30, s93, 12
	s_add_u32 s28, s26, s30
	s_addc_u32 s29, s27, 0
	global_load_dwordx2 v[74:75], v162, s[28:29]
	v_cvt_f32_ubyte0_e32 v140, v76
	v_cvt_f32_ubyte1_e32 v142, v76
	v_cvt_f32_ubyte2_e32 v144, v76
	v_cvt_f32_ubyte3_e32 v146, v76
	v_cvt_f32_ubyte0_e32 v148, v77
	v_cvt_f32_ubyte1_e32 v150, v77
	v_cvt_f32_ubyte2_e32 v152, v77
	v_cvt_f32_ubyte3_e32 v154, v77
	s_lshl_b32 s30, s94, 12
	s_add_u32 s28, s26, s30
	s_addc_u32 s29, s27, 0
	global_load_dwordx2 v[76:77], v162, s[28:29]
	v_cvt_f32_ubyte0_e32 v141, v78
	v_cvt_f32_ubyte1_e32 v143, v78
	v_cvt_f32_ubyte2_e32 v145, v78
	v_cvt_f32_ubyte3_e32 v147, v78
	v_cvt_f32_ubyte0_e32 v149, v79
	v_cvt_f32_ubyte1_e32 v151, v79
	v_cvt_f32_ubyte2_e32 v153, v79
	v_cvt_f32_ubyte3_e32 v155, v79
	s_lshl_b32 s30, s95, 12
	s_add_u32 s28, s26, s30
	s_addc_u32 s29, s27, 0
	global_load_dwordx2 v[78:79], v162, s[28:29]
	s_waitcnt vmcnt(29)
	v_cvt_f32_ubyte0_e32 v210, v80
	v_cvt_f32_ubyte1_e32 v212, v80
	v_cvt_f32_ubyte2_e32 v214, v80
	v_cvt_f32_ubyte3_e32 v216, v80
	v_cvt_f32_ubyte0_e32 v218, v81
	v_cvt_f32_ubyte1_e32 v220, v81
	v_cvt_f32_ubyte2_e32 v222, v81
	v_cvt_f32_ubyte3_e32 v224, v81
	s_lshl_b32 s30, s96, 12
	s_add_u32 s28, s26, s30
	s_addc_u32 s29, s27, 0
	global_load_dwordx2 v[80:81], v162, s[28:29]
	v_cvt_f32_ubyte0_e32 v211, v82
	v_cvt_f32_ubyte1_e32 v213, v82
	v_cvt_f32_ubyte2_e32 v215, v82
	v_cvt_f32_ubyte3_e32 v217, v82
	v_cvt_f32_ubyte0_e32 v219, v83
	v_cvt_f32_ubyte1_e32 v221, v83
	v_cvt_f32_ubyte2_e32 v223, v83
	v_cvt_f32_ubyte3_e32 v225, v83
	s_lshl_b32 s30, s97, 12
	s_add_u32 s28, s26, s30
	s_addc_u32 s29, s27, 0
	global_load_dwordx2 v[82:83], v162, s[28:29]
	v_cvt_f32_ubyte0_e32 v238, v84
	v_cvt_f32_ubyte1_e32 v240, v84
	v_cvt_f32_ubyte2_e32 v242, v84
	v_cvt_f32_ubyte3_e32 v244, v84
	v_cvt_f32_ubyte0_e32 v246, v85
	v_cvt_f32_ubyte1_e32 v248, v85
	v_cvt_f32_ubyte2_e32 v250, v85
	v_cvt_f32_ubyte3_e32 v252, v85
	s_lshl_b32 s30, s98, 12
	s_add_u32 s28, s26, s30
	s_addc_u32 s29, s27, 0
	global_load_dwordx2 v[84:85], v162, s[28:29]
	v_cvt_f32_ubyte0_e32 v239, v86
	v_cvt_f32_ubyte1_e32 v241, v86
	v_cvt_f32_ubyte2_e32 v243, v86
	v_cvt_f32_ubyte3_e32 v245, v86
	v_cvt_f32_ubyte0_e32 v247, v87
	v_cvt_f32_ubyte1_e32 v249, v87
	v_cvt_f32_ubyte2_e32 v251, v87
	v_cvt_f32_ubyte3_e32 v253, v87
	s_lshl_b32 s30, s99, 12
	s_add_u32 s28, s26, s30
	s_addc_u32 s29, s27, 0
	global_load_dwordx2 v[86:87], v162, s[28:29]
	v_mul_f32_e32 v202, v124, v108
	v_mul_f32_e32 v203, v125, v108
	v_mul_f32_e32 v204, v140, v108
	v_mul_f32_e32 v205, v141, v108
	v_mul_f32_e32 v206, v210, v108
	v_mul_f32_e32 v207, v211, v108
	v_mul_f32_e32 v208, v238, v108
	v_mul_f32_e32 v209, v239, v108
	v_fmac_f32_e32 v202, v126, v109
	v_fmac_f32_e32 v203, v127, v109
	v_fmac_f32_e32 v204, v142, v109
	v_fmac_f32_e32 v205, v143, v109
	v_fmac_f32_e32 v206, v212, v109
	v_fmac_f32_e32 v207, v213, v109
	v_fmac_f32_e32 v208, v240, v109
	v_fmac_f32_e32 v209, v241, v109
	v_fmac_f32_e32 v202, v128, v110
	v_fmac_f32_e32 v203, v129, v110
	v_fmac_f32_e32 v204, v144, v110
	v_fmac_f32_e32 v205, v145, v110
	v_fmac_f32_e32 v206, v214, v110
	v_fmac_f32_e32 v207, v215, v110
	v_fmac_f32_e32 v208, v242, v110
	v_fmac_f32_e32 v209, v243, v110
	v_fmac_f32_e32 v202, v130, v111
	v_fmac_f32_e32 v203, v131, v111
	v_fmac_f32_e32 v204, v146, v111
	v_fmac_f32_e32 v205, v147, v111
	v_fmac_f32_e32 v206, v216, v111
	v_fmac_f32_e32 v207, v217, v111
	v_fmac_f32_e32 v208, v244, v111
	v_fmac_f32_e32 v209, v245, v111
	v_fmac_f32_e32 v202, v132, v112
	v_fmac_f32_e32 v203, v133, v112
	v_fmac_f32_e32 v204, v148, v112
	v_fmac_f32_e32 v205, v149, v112
	v_fmac_f32_e32 v206, v218, v112
	v_fmac_f32_e32 v207, v219, v112
	v_fmac_f32_e32 v208, v246, v112
	v_fmac_f32_e32 v209, v247, v112
	v_fmac_f32_e32 v202, v134, v113
	v_fmac_f32_e32 v203, v135, v113
	v_fmac_f32_e32 v204, v150, v113
	v_fmac_f32_e32 v205, v151, v113
	v_fmac_f32_e32 v206, v220, v113
	v_fmac_f32_e32 v207, v221, v113
	v_fmac_f32_e32 v208, v248, v113
	v_fmac_f32_e32 v209, v249, v113
	v_fmac_f32_e32 v202, v136, v114
	v_fmac_f32_e32 v203, v137, v114
	v_fmac_f32_e32 v204, v152, v114
	v_fmac_f32_e32 v205, v153, v114
	v_fmac_f32_e32 v206, v222, v114
	v_fmac_f32_e32 v207, v223, v114
	v_fmac_f32_e32 v208, v250, v114
	v_fmac_f32_e32 v209, v251, v114
	v_fmac_f32_e32 v202, v138, v115
	v_fmac_f32_e32 v203, v139, v115
	v_fmac_f32_e32 v204, v154, v115
	v_fmac_f32_e32 v205, v155, v115
	v_fmac_f32_e32 v206, v224, v115
	v_fmac_f32_e32 v207, v225, v115
	v_fmac_f32_e32 v208, v252, v115
	v_fmac_f32_e32 v209, v253, v115
	v_permlane32_swap_b32_e32 v178, v194
	v_permlane32_swap_b32_e32 v179, v195
	v_permlane32_swap_b32_e32 v180, v196
	v_permlane32_swap_b32_e32 v181, v197
	v_permlane32_swap_b32_e32 v182, v198
	v_permlane32_swap_b32_e32 v183, v199
	v_permlane32_swap_b32_e32 v184, v200
	v_permlane32_swap_b32_e32 v185, v201
	v_permlane32_swap_b32_e32 v186, v202
	v_permlane32_swap_b32_e32 v187, v203
	v_permlane32_swap_b32_e32 v188, v204
	v_permlane32_swap_b32_e32 v189, v205
	v_permlane32_swap_b32_e32 v190, v206
	v_permlane32_swap_b32_e32 v191, v207
	v_permlane32_swap_b32_e32 v192, v208
	v_permlane32_swap_b32_e32 v193, v209
	v_add_f32_e32 v178, v178, v194
	v_add_f32_e32 v179, v179, v195
	v_add_f32_e32 v180, v180, v196
	v_add_f32_e32 v181, v181, v197
	v_add_f32_e32 v182, v182, v198
	v_add_f32_e32 v183, v183, v199
	v_add_f32_e32 v184, v184, v200
	v_add_f32_e32 v185, v185, v201
	v_add_f32_e32 v186, v186, v202
	v_add_f32_e32 v187, v187, v203
	v_add_f32_e32 v188, v188, v204
	v_add_f32_e32 v189, v189, v205
	v_add_f32_e32 v190, v190, v206
	v_add_f32_e32 v191, v191, v207
	v_add_f32_e32 v192, v192, v208
	v_add_f32_e32 v193, v193, v209
	v_permlane16_swap_b32_e32 v178, v186
	v_permlane16_swap_b32_e32 v179, v187
	v_permlane16_swap_b32_e32 v180, v188
	v_permlane16_swap_b32_e32 v181, v189
	v_permlane16_swap_b32_e32 v182, v190
	v_permlane16_swap_b32_e32 v183, v191
	v_permlane16_swap_b32_e32 v184, v192
	v_permlane16_swap_b32_e32 v185, v193
	v_add_f32_e32 v178, v178, v186
	v_add_f32_e32 v179, v179, v187
	v_add_f32_e32 v180, v180, v188
	v_add_f32_e32 v181, v181, v189
	v_add_f32_e32 v182, v182, v190
	v_add_f32_e32 v183, v183, v191
	v_add_f32_e32 v184, v184, v192
	v_add_f32_e32 v185, v185, v193
	v_cndmask_b32_e64 v2, v178, v182, s[8:9]
	v_cndmask_b32_e64 v3, v179, v183, s[8:9]
	v_cndmask_b32_e64 v4, v180, v184, s[8:9]
	v_cndmask_b32_e64 v5, v181, v185, s[8:9]
	v_cndmask_b32_e64 v6, v182, v178, s[8:9]
	v_cndmask_b32_e64 v7, v183, v179, s[8:9]
	v_cndmask_b32_e64 v8, v184, v180, s[8:9]
	v_cndmask_b32_e64 v9, v185, v181, s[8:9]
	v_add_f32_dpp v6, v2, v6 row_ror:8 row_mask:0xf bank_mask:0xf
	v_add_f32_dpp v7, v3, v7 row_ror:8 row_mask:0xf bank_mask:0xf
	v_add_f32_dpp v8, v4, v8 row_ror:8 row_mask:0xf bank_mask:0xf
	v_add_f32_dpp v9, v5, v9 row_ror:8 row_mask:0xf bank_mask:0xf
	v_cndmask_b32_e64 v2, v6, v8, s[10:11]
	v_cndmask_b32_e64 v3, v7, v9, s[10:11]
	v_cndmask_b32_e64 v4, v8, v6, s[10:11]
	v_cndmask_b32_e64 v5, v9, v7, s[10:11]
	v_add_f32_dpp v4, v2, v4 row_half_mirror row_mask:0xf bank_mask:0xf
	v_add_f32_dpp v5, v3, v5 row_half_mirror row_mask:0xf bank_mask:0xf
	v_cndmask_b32_e64 v2, v4, v5, s[14:15]
	v_cndmask_b32_e64 v3, v5, v4, s[14:15]
	s_nop 0
	v_add_f32_dpp v3, v2, v3 quad_perm:[2,3,0,1] row_mask:0xf bank_mask:0xf
	s_nop 1
	v_add_f32_dpp v11, v3, v3 quad_perm:[1,0,3,2] row_mask:0xf bank_mask:0xf
	s_mov_b64 exec, s[2:3]
	global_store_dword v[22:23], v11, off offset:256
	s_mov_b64 exec, -1
	s_waitcnt vmcnt(29)
	v_cvt_f32_ubyte0_e32 v124, v24
	v_cvt_f32_ubyte1_e32 v126, v24
	v_cvt_f32_ubyte2_e32 v128, v24
	v_cvt_f32_ubyte3_e32 v130, v24
	v_cvt_f32_ubyte0_e32 v132, v25
	v_cvt_f32_ubyte1_e32 v134, v25
	v_cvt_f32_ubyte2_e32 v136, v25
	v_cvt_f32_ubyte3_e32 v138, v25
	v_cvt_f32_ubyte0_e32 v125, v26
	v_cvt_f32_ubyte1_e32 v127, v26
	v_cvt_f32_ubyte2_e32 v129, v26
	v_cvt_f32_ubyte3_e32 v131, v26
	v_cvt_f32_ubyte0_e32 v133, v27
	v_cvt_f32_ubyte1_e32 v135, v27
	v_cvt_f32_ubyte2_e32 v137, v27
	v_cvt_f32_ubyte3_e32 v139, v27
	v_cvt_f32_ubyte0_e32 v140, v28
	v_cvt_f32_ubyte1_e32 v142, v28
	v_cvt_f32_ubyte2_e32 v144, v28
	v_cvt_f32_ubyte3_e32 v146, v28
	v_cvt_f32_ubyte0_e32 v148, v29
	v_cvt_f32_ubyte1_e32 v150, v29
	v_cvt_f32_ubyte2_e32 v152, v29
	v_cvt_f32_ubyte3_e32 v154, v29
	v_cvt_f32_ubyte0_e32 v141, v30
	v_cvt_f32_ubyte1_e32 v143, v30
	v_cvt_f32_ubyte2_e32 v145, v30
	v_cvt_f32_ubyte3_e32 v147, v30
	v_cvt_f32_ubyte0_e32 v149, v31
	v_cvt_f32_ubyte1_e32 v151, v31
	v_cvt_f32_ubyte2_e32 v153, v31
	v_cvt_f32_ubyte3_e32 v155, v31
	s_waitcnt vmcnt(25)
	v_cvt_f32_ubyte0_e32 v210, v32
	v_cvt_f32_ubyte1_e32 v212, v32
	v_cvt_f32_ubyte2_e32 v214, v32
	v_cvt_f32_ubyte3_e32 v216, v32
	v_cvt_f32_ubyte0_e32 v218, v33
	v_cvt_f32_ubyte1_e32 v220, v33
	v_cvt_f32_ubyte2_e32 v222, v33
	v_cvt_f32_ubyte3_e32 v224, v33
	v_cvt_f32_ubyte0_e32 v211, v34
	v_cvt_f32_ubyte1_e32 v213, v34
	v_cvt_f32_ubyte2_e32 v215, v34
	v_cvt_f32_ubyte3_e32 v217, v34
	v_cvt_f32_ubyte0_e32 v219, v35
	v_cvt_f32_ubyte1_e32 v221, v35
	v_cvt_f32_ubyte2_e32 v223, v35
	v_cvt_f32_ubyte3_e32 v225, v35
	v_cvt_f32_ubyte0_e32 v238, v36
	v_cvt_f32_ubyte1_e32 v240, v36
	v_cvt_f32_ubyte2_e32 v242, v36
	v_cvt_f32_ubyte3_e32 v244, v36
	v_cvt_f32_ubyte0_e32 v246, v37
	v_cvt_f32_ubyte1_e32 v248, v37
	v_cvt_f32_ubyte2_e32 v250, v37
	v_cvt_f32_ubyte3_e32 v252, v37
	v_cvt_f32_ubyte0_e32 v239, v38
	v_cvt_f32_ubyte1_e32 v241, v38
	v_cvt_f32_ubyte2_e32 v243, v38
	v_cvt_f32_ubyte3_e32 v245, v38
	v_cvt_f32_ubyte0_e32 v247, v39
	v_cvt_f32_ubyte1_e32 v249, v39
	v_cvt_f32_ubyte2_e32 v251, v39
	v_cvt_f32_ubyte3_e32 v253, v39
	v_mul_f32_e32 v178, v124, v108
	v_mul_f32_e32 v179, v125, v108
	v_mul_f32_e32 v180, v140, v108
	v_mul_f32_e32 v181, v141, v108
	v_mul_f32_e32 v182, v210, v108
	v_mul_f32_e32 v183, v211, v108
	v_mul_f32_e32 v184, v238, v108
	v_mul_f32_e32 v185, v239, v108
	v_fmac_f32_e32 v178, v126, v109
	v_fmac_f32_e32 v179, v127, v109
	v_fmac_f32_e32 v180, v142, v109
	v_fmac_f32_e32 v181, v143, v109
	v_fmac_f32_e32 v182, v212, v109
	v_fmac_f32_e32 v183, v213, v109
	v_fmac_f32_e32 v184, v240, v109
	v_fmac_f32_e32 v185, v241, v109
	v_fmac_f32_e32 v178, v128, v110
	v_fmac_f32_e32 v179, v129, v110
	v_fmac_f32_e32 v180, v144, v110
	v_fmac_f32_e32 v181, v145, v110
	v_fmac_f32_e32 v182, v214, v110
	v_fmac_f32_e32 v183, v215, v110
	v_fmac_f32_e32 v184, v242, v110
	v_fmac_f32_e32 v185, v243, v110
	v_fmac_f32_e32 v178, v130, v111
	v_fmac_f32_e32 v179, v131, v111
	v_fmac_f32_e32 v180, v146, v111
	v_fmac_f32_e32 v181, v147, v111
	v_fmac_f32_e32 v182, v216, v111
	v_fmac_f32_e32 v183, v217, v111
	v_fmac_f32_e32 v184, v244, v111
	v_fmac_f32_e32 v185, v245, v111
	v_fmac_f32_e32 v178, v132, v112
	v_fmac_f32_e32 v179, v133, v112
	v_fmac_f32_e32 v180, v148, v112
	v_fmac_f32_e32 v181, v149, v112
	v_fmac_f32_e32 v182, v218, v112
	v_fmac_f32_e32 v183, v219, v112
	v_fmac_f32_e32 v184, v246, v112
	v_fmac_f32_e32 v185, v247, v112
	v_fmac_f32_e32 v178, v134, v113
	v_fmac_f32_e32 v179, v135, v113
	v_fmac_f32_e32 v180, v150, v113
	v_fmac_f32_e32 v181, v151, v113
	v_fmac_f32_e32 v182, v220, v113
	v_fmac_f32_e32 v183, v221, v113
	v_fmac_f32_e32 v184, v248, v113
	v_fmac_f32_e32 v185, v249, v113
	v_fmac_f32_e32 v178, v136, v114
	v_fmac_f32_e32 v179, v137, v114
	v_fmac_f32_e32 v180, v152, v114
	v_fmac_f32_e32 v181, v153, v114
	v_fmac_f32_e32 v182, v222, v114
	v_fmac_f32_e32 v183, v223, v114
	v_fmac_f32_e32 v184, v250, v114
	v_fmac_f32_e32 v185, v251, v114
	v_fmac_f32_e32 v178, v138, v115
	v_fmac_f32_e32 v179, v139, v115
	v_fmac_f32_e32 v180, v154, v115
	v_fmac_f32_e32 v181, v155, v115
	v_fmac_f32_e32 v182, v224, v115
	v_fmac_f32_e32 v183, v225, v115
	v_fmac_f32_e32 v184, v252, v115
	v_fmac_f32_e32 v185, v253, v115
	s_waitcnt vmcnt(21)
	v_cvt_f32_ubyte0_e32 v124, v40
	v_cvt_f32_ubyte1_e32 v126, v40
	v_cvt_f32_ubyte2_e32 v128, v40
	v_cvt_f32_ubyte3_e32 v130, v40
	v_cvt_f32_ubyte0_e32 v132, v41
	v_cvt_f32_ubyte1_e32 v134, v41
	v_cvt_f32_ubyte2_e32 v136, v41
	v_cvt_f32_ubyte3_e32 v138, v41
	v_cvt_f32_ubyte0_e32 v125, v42
	v_cvt_f32_ubyte1_e32 v127, v42
	v_cvt_f32_ubyte2_e32 v129, v42
	v_cvt_f32_ubyte3_e32 v131, v42
	v_cvt_f32_ubyte0_e32 v133, v43
	v_cvt_f32_ubyte1_e32 v135, v43
	v_cvt_f32_ubyte2_e32 v137, v43
	v_cvt_f32_ubyte3_e32 v139, v43
	v_cvt_f32_ubyte0_e32 v140, v44
	v_cvt_f32_ubyte1_e32 v142, v44
	v_cvt_f32_ubyte2_e32 v144, v44
	v_cvt_f32_ubyte3_e32 v146, v44
	v_cvt_f32_ubyte0_e32 v148, v45
	v_cvt_f32_ubyte1_e32 v150, v45
	v_cvt_f32_ubyte2_e32 v152, v45
	v_cvt_f32_ubyte3_e32 v154, v45
	v_cvt_f32_ubyte0_e32 v141, v46
	v_cvt_f32_ubyte1_e32 v143, v46
	v_cvt_f32_ubyte2_e32 v145, v46
	v_cvt_f32_ubyte3_e32 v147, v46
	v_cvt_f32_ubyte0_e32 v149, v47
	v_cvt_f32_ubyte1_e32 v151, v47
	v_cvt_f32_ubyte2_e32 v153, v47
	v_cvt_f32_ubyte3_e32 v155, v47
	s_waitcnt vmcnt(17)
	v_cvt_f32_ubyte0_e32 v210, v48
	v_cvt_f32_ubyte1_e32 v212, v48
	v_cvt_f32_ubyte2_e32 v214, v48
	v_cvt_f32_ubyte3_e32 v216, v48
	v_cvt_f32_ubyte0_e32 v218, v49
	v_cvt_f32_ubyte1_e32 v220, v49
	v_cvt_f32_ubyte2_e32 v222, v49
	v_cvt_f32_ubyte3_e32 v224, v49
	v_cvt_f32_ubyte0_e32 v211, v50
	v_cvt_f32_ubyte1_e32 v213, v50
	v_cvt_f32_ubyte2_e32 v215, v50
	v_cvt_f32_ubyte3_e32 v217, v50
	v_cvt_f32_ubyte0_e32 v219, v51
	v_cvt_f32_ubyte1_e32 v221, v51
	v_cvt_f32_ubyte2_e32 v223, v51
	v_cvt_f32_ubyte3_e32 v225, v51
	v_cvt_f32_ubyte0_e32 v238, v52
	v_cvt_f32_ubyte1_e32 v240, v52
	v_cvt_f32_ubyte2_e32 v242, v52
	v_cvt_f32_ubyte3_e32 v244, v52
	v_cvt_f32_ubyte0_e32 v246, v53
	v_cvt_f32_ubyte1_e32 v248, v53
	v_cvt_f32_ubyte2_e32 v250, v53
	v_cvt_f32_ubyte3_e32 v252, v53
	v_cvt_f32_ubyte0_e32 v239, v54
	v_cvt_f32_ubyte1_e32 v241, v54
	v_cvt_f32_ubyte2_e32 v243, v54
	v_cvt_f32_ubyte3_e32 v245, v54
	v_cvt_f32_ubyte0_e32 v247, v55
	v_cvt_f32_ubyte1_e32 v249, v55
	v_cvt_f32_ubyte2_e32 v251, v55
	v_cvt_f32_ubyte3_e32 v253, v55
	v_mul_f32_e32 v186, v124, v108
	v_mul_f32_e32 v187, v125, v108
	v_mul_f32_e32 v188, v140, v108
	v_mul_f32_e32 v189, v141, v108
	v_mul_f32_e32 v190, v210, v108
	v_mul_f32_e32 v191, v211, v108
	v_mul_f32_e32 v192, v238, v108
	v_mul_f32_e32 v193, v239, v108
	v_fmac_f32_e32 v186, v126, v109
	v_fmac_f32_e32 v187, v127, v109
	v_fmac_f32_e32 v188, v142, v109
	v_fmac_f32_e32 v189, v143, v109
	v_fmac_f32_e32 v190, v212, v109
	v_fmac_f32_e32 v191, v213, v109
	v_fmac_f32_e32 v192, v240, v109
	v_fmac_f32_e32 v193, v241, v109
	v_fmac_f32_e32 v186, v128, v110
	v_fmac_f32_e32 v187, v129, v110
	v_fmac_f32_e32 v188, v144, v110
	v_fmac_f32_e32 v189, v145, v110
	v_fmac_f32_e32 v190, v214, v110
	v_fmac_f32_e32 v191, v215, v110
	v_fmac_f32_e32 v192, v242, v110
	v_fmac_f32_e32 v193, v243, v110
	v_fmac_f32_e32 v186, v130, v111
	v_fmac_f32_e32 v187, v131, v111
	v_fmac_f32_e32 v188, v146, v111
	v_fmac_f32_e32 v189, v147, v111
	v_fmac_f32_e32 v190, v216, v111
	v_fmac_f32_e32 v191, v217, v111
	v_fmac_f32_e32 v192, v244, v111
	v_fmac_f32_e32 v193, v245, v111
	v_fmac_f32_e32 v186, v132, v112
	v_fmac_f32_e32 v187, v133, v112
	v_fmac_f32_e32 v188, v148, v112
	v_fmac_f32_e32 v189, v149, v112
	v_fmac_f32_e32 v190, v218, v112
	v_fmac_f32_e32 v191, v219, v112
	v_fmac_f32_e32 v192, v246, v112
	v_fmac_f32_e32 v193, v247, v112
	v_fmac_f32_e32 v186, v134, v113
	v_fmac_f32_e32 v187, v135, v113
	v_fmac_f32_e32 v188, v150, v113
	v_fmac_f32_e32 v189, v151, v113
	v_fmac_f32_e32 v190, v220, v113
	v_fmac_f32_e32 v191, v221, v113
	v_fmac_f32_e32 v192, v248, v113
	v_fmac_f32_e32 v193, v249, v113
	v_fmac_f32_e32 v186, v136, v114
	v_fmac_f32_e32 v187, v137, v114
	v_fmac_f32_e32 v188, v152, v114
	v_fmac_f32_e32 v189, v153, v114
	v_fmac_f32_e32 v190, v222, v114
	v_fmac_f32_e32 v191, v223, v114
	v_fmac_f32_e32 v192, v250, v114
	v_fmac_f32_e32 v193, v251, v114
	v_fmac_f32_e32 v186, v138, v115
	v_fmac_f32_e32 v187, v139, v115
	v_fmac_f32_e32 v188, v154, v115
	v_fmac_f32_e32 v189, v155, v115
	v_fmac_f32_e32 v190, v224, v115
	v_fmac_f32_e32 v191, v225, v115
	v_fmac_f32_e32 v192, v252, v115
	v_fmac_f32_e32 v193, v253, v115
	s_waitcnt vmcnt(13)
	v_cvt_f32_ubyte0_e32 v124, v56
	v_cvt_f32_ubyte1_e32 v126, v56
	v_cvt_f32_ubyte2_e32 v128, v56
	v_cvt_f32_ubyte3_e32 v130, v56
	v_cvt_f32_ubyte0_e32 v132, v57
	v_cvt_f32_ubyte1_e32 v134, v57
	v_cvt_f32_ubyte2_e32 v136, v57
	v_cvt_f32_ubyte3_e32 v138, v57
	v_cvt_f32_ubyte0_e32 v125, v58
	v_cvt_f32_ubyte1_e32 v127, v58
	v_cvt_f32_ubyte2_e32 v129, v58
	v_cvt_f32_ubyte3_e32 v131, v58
	v_cvt_f32_ubyte0_e32 v133, v59
	v_cvt_f32_ubyte1_e32 v135, v59
	v_cvt_f32_ubyte2_e32 v137, v59
	v_cvt_f32_ubyte3_e32 v139, v59
	v_cvt_f32_ubyte0_e32 v140, v60
	v_cvt_f32_ubyte1_e32 v142, v60
	v_cvt_f32_ubyte2_e32 v144, v60
	v_cvt_f32_ubyte3_e32 v146, v60
	v_cvt_f32_ubyte0_e32 v148, v61
	v_cvt_f32_ubyte1_e32 v150, v61
	v_cvt_f32_ubyte2_e32 v152, v61
	v_cvt_f32_ubyte3_e32 v154, v61
	v_cvt_f32_ubyte0_e32 v141, v62
	v_cvt_f32_ubyte1_e32 v143, v62
	v_cvt_f32_ubyte2_e32 v145, v62
	v_cvt_f32_ubyte3_e32 v147, v62
	v_cvt_f32_ubyte0_e32 v149, v63
	v_cvt_f32_ubyte1_e32 v151, v63
	v_cvt_f32_ubyte2_e32 v153, v63
	v_cvt_f32_ubyte3_e32 v155, v63
	s_waitcnt vmcnt(9)
	v_cvt_f32_ubyte0_e32 v210, v64
	v_cvt_f32_ubyte1_e32 v212, v64
	v_cvt_f32_ubyte2_e32 v214, v64
	v_cvt_f32_ubyte3_e32 v216, v64
	v_cvt_f32_ubyte0_e32 v218, v65
	v_cvt_f32_ubyte1_e32 v220, v65
	v_cvt_f32_ubyte2_e32 v222, v65
	v_cvt_f32_ubyte3_e32 v224, v65
	v_cvt_f32_ubyte0_e32 v211, v66
	v_cvt_f32_ubyte1_e32 v213, v66
	v_cvt_f32_ubyte2_e32 v215, v66
	v_cvt_f32_ubyte3_e32 v217, v66
	v_cvt_f32_ubyte0_e32 v219, v67
	v_cvt_f32_ubyte1_e32 v221, v67
	v_cvt_f32_ubyte2_e32 v223, v67
	v_cvt_f32_ubyte3_e32 v225, v67
	v_cvt_f32_ubyte0_e32 v238, v68
	v_cvt_f32_ubyte1_e32 v240, v68
	v_cvt_f32_ubyte2_e32 v242, v68
	v_cvt_f32_ubyte3_e32 v244, v68
	v_cvt_f32_ubyte0_e32 v246, v69
	v_cvt_f32_ubyte1_e32 v248, v69
	v_cvt_f32_ubyte2_e32 v250, v69
	v_cvt_f32_ubyte3_e32 v252, v69
	v_cvt_f32_ubyte0_e32 v239, v70
	v_cvt_f32_ubyte1_e32 v241, v70
	v_cvt_f32_ubyte2_e32 v243, v70
	v_cvt_f32_ubyte3_e32 v245, v70
	v_cvt_f32_ubyte0_e32 v247, v71
	v_cvt_f32_ubyte1_e32 v249, v71
	v_cvt_f32_ubyte2_e32 v251, v71
	v_cvt_f32_ubyte3_e32 v253, v71
	v_mul_f32_e32 v194, v124, v108
	v_mul_f32_e32 v195, v125, v108
	v_mul_f32_e32 v196, v140, v108
	v_mul_f32_e32 v197, v141, v108
	v_mul_f32_e32 v198, v210, v108
	v_mul_f32_e32 v199, v211, v108
	v_mul_f32_e32 v200, v238, v108
	v_mul_f32_e32 v201, v239, v108
	v_fmac_f32_e32 v194, v126, v109
	v_fmac_f32_e32 v195, v127, v109
	v_fmac_f32_e32 v196, v142, v109
	v_fmac_f32_e32 v197, v143, v109
	v_fmac_f32_e32 v198, v212, v109
	v_fmac_f32_e32 v199, v213, v109
	v_fmac_f32_e32 v200, v240, v109
	v_fmac_f32_e32 v201, v241, v109
	v_fmac_f32_e32 v194, v128, v110
	v_fmac_f32_e32 v195, v129, v110
	v_fmac_f32_e32 v196, v144, v110
	v_fmac_f32_e32 v197, v145, v110
	v_fmac_f32_e32 v198, v214, v110
	v_fmac_f32_e32 v199, v215, v110
	v_fmac_f32_e32 v200, v242, v110
	v_fmac_f32_e32 v201, v243, v110
	v_fmac_f32_e32 v194, v130, v111
	v_fmac_f32_e32 v195, v131, v111
	v_fmac_f32_e32 v196, v146, v111
	v_fmac_f32_e32 v197, v147, v111
	v_fmac_f32_e32 v198, v216, v111
	v_fmac_f32_e32 v199, v217, v111
	v_fmac_f32_e32 v200, v244, v111
	v_fmac_f32_e32 v201, v245, v111
	v_fmac_f32_e32 v194, v132, v112
	v_fmac_f32_e32 v195, v133, v112
	v_fmac_f32_e32 v196, v148, v112
	v_fmac_f32_e32 v197, v149, v112
	v_fmac_f32_e32 v198, v218, v112
	v_fmac_f32_e32 v199, v219, v112
	v_fmac_f32_e32 v200, v246, v112
	v_fmac_f32_e32 v201, v247, v112
	v_fmac_f32_e32 v194, v134, v113
	v_fmac_f32_e32 v195, v135, v113
	v_fmac_f32_e32 v196, v150, v113
	v_fmac_f32_e32 v197, v151, v113
	v_fmac_f32_e32 v198, v220, v113
	v_fmac_f32_e32 v199, v221, v113
	v_fmac_f32_e32 v200, v248, v113
	v_fmac_f32_e32 v201, v249, v113
	v_fmac_f32_e32 v194, v136, v114
	v_fmac_f32_e32 v195, v137, v114
	v_fmac_f32_e32 v196, v152, v114
	v_fmac_f32_e32 v197, v153, v114
	v_fmac_f32_e32 v198, v222, v114
	v_fmac_f32_e32 v199, v223, v114
	v_fmac_f32_e32 v200, v250, v114
	v_fmac_f32_e32 v201, v251, v114
	v_fmac_f32_e32 v194, v138, v115
	v_fmac_f32_e32 v195, v139, v115
	v_fmac_f32_e32 v196, v154, v115
	v_fmac_f32_e32 v197, v155, v115
	v_fmac_f32_e32 v198, v224, v115
	v_fmac_f32_e32 v199, v225, v115
	v_fmac_f32_e32 v200, v252, v115
	v_fmac_f32_e32 v201, v253, v115
	s_waitcnt vmcnt(5)
	v_cvt_f32_ubyte0_e32 v124, v72
	v_cvt_f32_ubyte1_e32 v126, v72
	v_cvt_f32_ubyte2_e32 v128, v72
	v_cvt_f32_ubyte3_e32 v130, v72
	v_cvt_f32_ubyte0_e32 v132, v73
	v_cvt_f32_ubyte1_e32 v134, v73
	v_cvt_f32_ubyte2_e32 v136, v73
	v_cvt_f32_ubyte3_e32 v138, v73
	v_cvt_f32_ubyte0_e32 v125, v74
	v_cvt_f32_ubyte1_e32 v127, v74
	v_cvt_f32_ubyte2_e32 v129, v74
	v_cvt_f32_ubyte3_e32 v131, v74
	v_cvt_f32_ubyte0_e32 v133, v75
	v_cvt_f32_ubyte1_e32 v135, v75
	v_cvt_f32_ubyte2_e32 v137, v75
	v_cvt_f32_ubyte3_e32 v139, v75
	v_cvt_f32_ubyte0_e32 v140, v76
	v_cvt_f32_ubyte1_e32 v142, v76
	v_cvt_f32_ubyte2_e32 v144, v76
	v_cvt_f32_ubyte3_e32 v146, v76
	v_cvt_f32_ubyte0_e32 v148, v77
	v_cvt_f32_ubyte1_e32 v150, v77
	v_cvt_f32_ubyte2_e32 v152, v77
	v_cvt_f32_ubyte3_e32 v154, v77
	v_cvt_f32_ubyte0_e32 v141, v78
	v_cvt_f32_ubyte1_e32 v143, v78
	v_cvt_f32_ubyte2_e32 v145, v78
	v_cvt_f32_ubyte3_e32 v147, v78
	v_cvt_f32_ubyte0_e32 v149, v79
	v_cvt_f32_ubyte1_e32 v151, v79
	v_cvt_f32_ubyte2_e32 v153, v79
	v_cvt_f32_ubyte3_e32 v155, v79
	s_waitcnt vmcnt(1)
	v_cvt_f32_ubyte0_e32 v210, v80
	v_cvt_f32_ubyte1_e32 v212, v80
	v_cvt_f32_ubyte2_e32 v214, v80
	v_cvt_f32_ubyte3_e32 v216, v80
	v_cvt_f32_ubyte0_e32 v218, v81
	v_cvt_f32_ubyte1_e32 v220, v81
	v_cvt_f32_ubyte2_e32 v222, v81
	v_cvt_f32_ubyte3_e32 v224, v81
	v_cvt_f32_ubyte0_e32 v211, v82
	v_cvt_f32_ubyte1_e32 v213, v82
	v_cvt_f32_ubyte2_e32 v215, v82
	v_cvt_f32_ubyte3_e32 v217, v82
	v_cvt_f32_ubyte0_e32 v219, v83
	v_cvt_f32_ubyte1_e32 v221, v83
	v_cvt_f32_ubyte2_e32 v223, v83
	v_cvt_f32_ubyte3_e32 v225, v83
	v_cvt_f32_ubyte0_e32 v238, v84
	v_cvt_f32_ubyte1_e32 v240, v84
	v_cvt_f32_ubyte2_e32 v242, v84
	v_cvt_f32_ubyte3_e32 v244, v84
	v_cvt_f32_ubyte0_e32 v246, v85
	v_cvt_f32_ubyte1_e32 v248, v85
	v_cvt_f32_ubyte2_e32 v250, v85
	v_cvt_f32_ubyte3_e32 v252, v85
	v_cvt_f32_ubyte0_e32 v239, v86
	v_cvt_f32_ubyte1_e32 v241, v86
	v_cvt_f32_ubyte2_e32 v243, v86
	v_cvt_f32_ubyte3_e32 v245, v86
	v_cvt_f32_ubyte0_e32 v247, v87
	v_cvt_f32_ubyte1_e32 v249, v87
	v_cvt_f32_ubyte2_e32 v251, v87
	v_cvt_f32_ubyte3_e32 v253, v87
	v_mul_f32_e32 v202, v124, v108
	v_mul_f32_e32 v203, v125, v108
	v_mul_f32_e32 v204, v140, v108
	v_mul_f32_e32 v205, v141, v108
	v_mul_f32_e32 v206, v210, v108
	v_mul_f32_e32 v207, v211, v108
	v_mul_f32_e32 v208, v238, v108
	v_mul_f32_e32 v209, v239, v108
	v_fmac_f32_e32 v202, v126, v109
	v_fmac_f32_e32 v203, v127, v109
	v_fmac_f32_e32 v204, v142, v109
	v_fmac_f32_e32 v205, v143, v109
	v_fmac_f32_e32 v206, v212, v109
	v_fmac_f32_e32 v207, v213, v109
	v_fmac_f32_e32 v208, v240, v109
	v_fmac_f32_e32 v209, v241, v109
	v_fmac_f32_e32 v202, v128, v110
	v_fmac_f32_e32 v203, v129, v110
	v_fmac_f32_e32 v204, v144, v110
	v_fmac_f32_e32 v205, v145, v110
	v_fmac_f32_e32 v206, v214, v110
	v_fmac_f32_e32 v207, v215, v110
	v_fmac_f32_e32 v208, v242, v110
	v_fmac_f32_e32 v209, v243, v110
	v_fmac_f32_e32 v202, v130, v111
	v_fmac_f32_e32 v203, v131, v111
	v_fmac_f32_e32 v204, v146, v111
	v_fmac_f32_e32 v205, v147, v111
	v_fmac_f32_e32 v206, v216, v111
	v_fmac_f32_e32 v207, v217, v111
	v_fmac_f32_e32 v208, v244, v111
	v_fmac_f32_e32 v209, v245, v111
	v_fmac_f32_e32 v202, v132, v112
	v_fmac_f32_e32 v203, v133, v112
	v_fmac_f32_e32 v204, v148, v112
	v_fmac_f32_e32 v205, v149, v112
	v_fmac_f32_e32 v206, v218, v112
	v_fmac_f32_e32 v207, v219, v112
	v_fmac_f32_e32 v208, v246, v112
	v_fmac_f32_e32 v209, v247, v112
	v_fmac_f32_e32 v202, v134, v113
	v_fmac_f32_e32 v203, v135, v113
	v_fmac_f32_e32 v204, v150, v113
	v_fmac_f32_e32 v205, v151, v113
	v_fmac_f32_e32 v206, v220, v113
	v_fmac_f32_e32 v207, v221, v113
	v_fmac_f32_e32 v208, v248, v113
	v_fmac_f32_e32 v209, v249, v113
	v_fmac_f32_e32 v202, v136, v114
	v_fmac_f32_e32 v203, v137, v114
	v_fmac_f32_e32 v204, v152, v114
	v_fmac_f32_e32 v205, v153, v114
	v_fmac_f32_e32 v206, v222, v114
	v_fmac_f32_e32 v207, v223, v114
	v_fmac_f32_e32 v208, v250, v114
	v_fmac_f32_e32 v209, v251, v114
	v_fmac_f32_e32 v202, v138, v115
	v_fmac_f32_e32 v203, v139, v115
	v_fmac_f32_e32 v204, v154, v115
	v_fmac_f32_e32 v205, v155, v115
	v_fmac_f32_e32 v206, v224, v115
	v_fmac_f32_e32 v207, v225, v115
	v_fmac_f32_e32 v208, v252, v115
	v_fmac_f32_e32 v209, v253, v115
	s_waitcnt lgkmcnt(0)
	s_load_dwordx16 s[84:99], s[38:39], 0x40 glc
	s_lshl_b32 s30, s68, 12
	s_add_u32 s28, s26, s30
	s_addc_u32 s29, s27, 0
	global_load_dwordx2 v[24:25], v162, s[28:29]
	s_lshl_b32 s30, s69, 12
	s_add_u32 s28, s26, s30
	s_addc_u32 s29, s27, 0
	global_load_dwordx2 v[26:27], v162, s[28:29]
	s_lshl_b32 s30, s70, 12
	s_add_u32 s28, s26, s30
	s_addc_u32 s29, s27, 0
	global_load_dwordx2 v[28:29], v162, s[28:29]
	s_lshl_b32 s30, s71, 12
	s_add_u32 s28, s26, s30
	s_addc_u32 s29, s27, 0
	global_load_dwordx2 v[30:31], v162, s[28:29]
	s_lshl_b32 s30, s72, 12
	s_add_u32 s28, s26, s30
	s_addc_u32 s29, s27, 0
	global_load_dwordx2 v[32:33], v162, s[28:29]
	s_lshl_b32 s30, s73, 12
	s_add_u32 s28, s26, s30
	s_addc_u32 s29, s27, 0
	global_load_dwordx2 v[34:35], v162, s[28:29]
	s_lshl_b32 s30, s74, 12
	s_add_u32 s28, s26, s30
	s_addc_u32 s29, s27, 0
	global_load_dwordx2 v[36:37], v162, s[28:29]
	s_lshl_b32 s30, s75, 12
	s_add_u32 s28, s26, s30
	s_addc_u32 s29, s27, 0
	global_load_dwordx2 v[38:39], v162, s[28:29]
	s_lshl_b32 s30, s76, 12
	s_add_u32 s28, s26, s30
	s_addc_u32 s29, s27, 0
	global_load_dwordx2 v[40:41], v162, s[28:29]
	s_lshl_b32 s30, s77, 12
	s_add_u32 s28, s26, s30
	s_addc_u32 s29, s27, 0
	global_load_dwordx2 v[42:43], v162, s[28:29]
	s_lshl_b32 s30, s78, 12
	s_add_u32 s28, s26, s30
	s_addc_u32 s29, s27, 0
	global_load_dwordx2 v[44:45], v162, s[28:29]
	s_lshl_b32 s30, s79, 12
	s_add_u32 s28, s26, s30
	s_addc_u32 s29, s27, 0
	global_load_dwordx2 v[46:47], v162, s[28:29]
	s_lshl_b32 s30, s80, 12
	s_add_u32 s28, s26, s30
	s_addc_u32 s29, s27, 0
	global_load_dwordx2 v[48:49], v162, s[28:29]
	s_lshl_b32 s30, s81, 12
	s_add_u32 s28, s26, s30
	s_addc_u32 s29, s27, 0
	global_load_dwordx2 v[50:51], v162, s[28:29]
	s_lshl_b32 s30, s82, 12
	s_add_u32 s28, s26, s30
	s_addc_u32 s29, s27, 0
	global_load_dwordx2 v[52:53], v162, s[28:29]
	s_lshl_b32 s30, s83, 12
	s_add_u32 s28, s26, s30
	s_addc_u32 s29, s27, 0
	global_load_dwordx2 v[54:55], v162, s[28:29]
	s_waitcnt lgkmcnt(0)
	s_load_dwordx16 s[68:83], s[38:39], 0x80 glc
	s_lshl_b32 s30, s84, 12
	s_add_u32 s28, s26, s30
	s_addc_u32 s29, s27, 0
	global_load_dwordx2 v[56:57], v162, s[28:29]
	s_lshl_b32 s30, s85, 12
	s_add_u32 s28, s26, s30
	s_addc_u32 s29, s27, 0
	global_load_dwordx2 v[58:59], v162, s[28:29]
	s_lshl_b32 s30, s86, 12
	s_add_u32 s28, s26, s30
	s_addc_u32 s29, s27, 0
	global_load_dwordx2 v[60:61], v162, s[28:29]
	s_lshl_b32 s30, s87, 12
	s_add_u32 s28, s26, s30
	s_addc_u32 s29, s27, 0
	global_load_dwordx2 v[62:63], v162, s[28:29]
	s_lshl_b32 s30, s88, 12
	s_add_u32 s28, s26, s30
	s_addc_u32 s29, s27, 0
	global_load_dwordx2 v[64:65], v162, s[28:29]
	s_lshl_b32 s30, s89, 12
	s_add_u32 s28, s26, s30
	s_addc_u32 s29, s27, 0
	global_load_dwordx2 v[66:67], v162, s[28:29]
	s_lshl_b32 s30, s90, 12
	s_add_u32 s28, s26, s30
	s_addc_u32 s29, s27, 0
	global_load_dwordx2 v[68:69], v162, s[28:29]
	s_lshl_b32 s30, s91, 12
	s_add_u32 s28, s26, s30
	s_addc_u32 s29, s27, 0
	global_load_dwordx2 v[70:71], v162, s[28:29]
	s_lshl_b32 s30, s92, 12
	s_add_u32 s28, s26, s30
	s_addc_u32 s29, s27, 0
	global_load_dwordx2 v[72:73], v162, s[28:29]
	s_lshl_b32 s30, s93, 12
	s_add_u32 s28, s26, s30
	s_addc_u32 s29, s27, 0
	global_load_dwordx2 v[74:75], v162, s[28:29]
	s_lshl_b32 s30, s94, 12
	s_add_u32 s28, s26, s30
	s_addc_u32 s29, s27, 0
	global_load_dwordx2 v[76:77], v162, s[28:29]
	s_lshl_b32 s30, s95, 12
	s_add_u32 s28, s26, s30
	s_addc_u32 s29, s27, 0
	global_load_dwordx2 v[78:79], v162, s[28:29]
	s_lshl_b32 s30, s96, 12
	s_add_u32 s28, s26, s30
	s_addc_u32 s29, s27, 0
	global_load_dwordx2 v[80:81], v162, s[28:29]
	s_lshl_b32 s30, s97, 12
	s_add_u32 s28, s26, s30
	s_addc_u32 s29, s27, 0
	global_load_dwordx2 v[82:83], v162, s[28:29]
	s_lshl_b32 s30, s98, 12
	s_add_u32 s28, s26, s30
	s_addc_u32 s29, s27, 0
	global_load_dwordx2 v[84:85], v162, s[28:29]
	s_lshl_b32 s30, s99, 12
	s_add_u32 s28, s26, s30
	s_addc_u32 s29, s27, 0
	global_load_dwordx2 v[86:87], v162, s[28:29]
	v_permlane32_swap_b32_e32 v178, v194
	v_permlane32_swap_b32_e32 v179, v195
	v_permlane32_swap_b32_e32 v180, v196
	v_permlane32_swap_b32_e32 v181, v197
	v_permlane32_swap_b32_e32 v182, v198
	v_permlane32_swap_b32_e32 v183, v199
	v_permlane32_swap_b32_e32 v184, v200
	v_permlane32_swap_b32_e32 v185, v201
	v_permlane32_swap_b32_e32 v186, v202
	v_permlane32_swap_b32_e32 v187, v203
	v_permlane32_swap_b32_e32 v188, v204
	v_permlane32_swap_b32_e32 v189, v205
	v_permlane32_swap_b32_e32 v190, v206
	v_permlane32_swap_b32_e32 v191, v207
	v_permlane32_swap_b32_e32 v192, v208
	v_permlane32_swap_b32_e32 v193, v209
	v_add_f32_e32 v178, v178, v194
	v_add_f32_e32 v179, v179, v195
	v_add_f32_e32 v180, v180, v196
	v_add_f32_e32 v181, v181, v197
	v_add_f32_e32 v182, v182, v198
	v_add_f32_e32 v183, v183, v199
	v_add_f32_e32 v184, v184, v200
	v_add_f32_e32 v185, v185, v201
	v_add_f32_e32 v186, v186, v202
	v_add_f32_e32 v187, v187, v203
	v_add_f32_e32 v188, v188, v204
	v_add_f32_e32 v189, v189, v205
	v_add_f32_e32 v190, v190, v206
	v_add_f32_e32 v191, v191, v207
	v_add_f32_e32 v192, v192, v208
	v_add_f32_e32 v193, v193, v209
	v_permlane16_swap_b32_e32 v178, v186
	v_permlane16_swap_b32_e32 v179, v187
	v_permlane16_swap_b32_e32 v180, v188
	v_permlane16_swap_b32_e32 v181, v189
	v_permlane16_swap_b32_e32 v182, v190
	v_permlane16_swap_b32_e32 v183, v191
	v_permlane16_swap_b32_e32 v184, v192
	v_permlane16_swap_b32_e32 v185, v193
	v_add_f32_e32 v178, v178, v186
	v_add_f32_e32 v179, v179, v187
	v_add_f32_e32 v180, v180, v188
	v_add_f32_e32 v181, v181, v189
	v_add_f32_e32 v182, v182, v190
	v_add_f32_e32 v183, v183, v191
	v_add_f32_e32 v184, v184, v192
	v_add_f32_e32 v185, v185, v193
	v_cndmask_b32_e64 v2, v178, v182, s[8:9]
	v_cndmask_b32_e64 v3, v179, v183, s[8:9]
	v_cndmask_b32_e64 v4, v180, v184, s[8:9]
	v_cndmask_b32_e64 v5, v181, v185, s[8:9]
	v_cndmask_b32_e64 v6, v182, v178, s[8:9]
	v_cndmask_b32_e64 v7, v183, v179, s[8:9]
	v_cndmask_b32_e64 v8, v184, v180, s[8:9]
	v_cndmask_b32_e64 v9, v185, v181, s[8:9]
	v_add_f32_dpp v6, v2, v6 row_ror:8 row_mask:0xf bank_mask:0xf
	v_add_f32_dpp v7, v3, v7 row_ror:8 row_mask:0xf bank_mask:0xf
	v_add_f32_dpp v8, v4, v8 row_ror:8 row_mask:0xf bank_mask:0xf
	v_add_f32_dpp v9, v5, v9 row_ror:8 row_mask:0xf bank_mask:0xf
	v_cndmask_b32_e64 v2, v6, v8, s[10:11]
	v_cndmask_b32_e64 v3, v7, v9, s[10:11]
	v_cndmask_b32_e64 v4, v8, v6, s[10:11]
	v_cndmask_b32_e64 v5, v9, v7, s[10:11]
	v_add_f32_dpp v4, v2, v4 row_half_mirror row_mask:0xf bank_mask:0xf
	v_add_f32_dpp v5, v3, v5 row_half_mirror row_mask:0xf bank_mask:0xf
	v_cndmask_b32_e64 v2, v4, v5, s[14:15]
	v_cndmask_b32_e64 v3, v5, v4, s[14:15]
	s_nop 0
	v_add_f32_dpp v3, v2, v3 quad_perm:[2,3,0,1] row_mask:0xf bank_mask:0xf
	s_nop 1
	v_add_f32_dpp v11, v3, v3 quad_perm:[1,0,3,2] row_mask:0xf bank_mask:0xf
	s_mov_b64 exec, s[2:3]
	global_store_dword v[22:23], v11, off offset:384
	s_mov_b64 exec, -1
	s_add_i32 s16, s16, 1
	s_cmp_lt_i32 s16, s17
	s_cbranch_scc1 .Lpa_tok
	s_waitcnt vmcnt(0)
	s_waitcnt vmcnt(0)
	v_cmp_eq_u32_e32 vcc, 0, v0
	s_waitcnt vmcnt(0) lgkmcnt(0)
	s_barrier
	s_and_saveexec_b64 s[2:3], vcc
	s_cbranch_execz .Lgbb_1444
	v_readlane_b32 s4, v237, 5
	s_waitcnt vmcnt(0) expcnt(0) lgkmcnt(0)
	s_nop 0
	v_mov_b32_e32 v1, s4
	ds_read_b32 v3, v1
	ds_read_b32 v1, v1 offset:4
	s_waitcnt lgkmcnt(1)
	v_cmp_ne_u32_e32 vcc, 0, v3
	s_branch .Lgbb_1412
	v_readlane_b32 s4, v237, 2
	v_readlane_b32 s5, v237, 3
	s_load_dwordx2 s[8:9], s[6:7], 0x4
	s_lshl_b64 s[4:5], s[4:5], 2
	v_readlane_b32 s6, v237, 0
	s_add_u32 s4, s6, s4
	v_readlane_b32 s6, v237, 1
	s_addc_u32 s5, s6, s5
	s_add_u32 s6, s4, 0x1000
	s_addc_u32 s7, s5, 0
	s_waitcnt lgkmcnt(0)
	s_mul_i32 s20, s8, s38
	s_add_u32 s8, s4, 0x1100
	s_mul_i32 s20, s20, s9
	s_addc_u32 s9, s5, 0
	s_add_u32 s10, s4, 0x1200
	s_addc_u32 s11, s5, 0
	s_add_u32 s12, s4, 0x1300
	s_addc_u32 s13, s5, 0
	s_mov_b32 s21, 1
	v_mov_b32_e32 v17, 0
	s_branch .Lgbb_1400
